# expert-weight conversion: bf16 output stores marked nt (written once, read phases later)
# speedup vs baseline: 1.0221x; 1.0130x over previous
; #define LAS __attribute__((address_space(3)))
; DI void conv_load(const ConvItem& c, f32x4 (&v)[8], int tid) {
; #pragma unroll
;     for (int i = 0; i < 8; ++i) { const int idx = tid + 512 * i, row = idx >> 6, c4 = idx & 63; v[i] = *(const f32x4*)(c.src + (size_t)(c.k0 + row) * c.ld + c.n0 + 4 * c4); }
; }
; DI void conv_store(const ConvItem& c, const f32x4 (&v)[8], LAS float* scr, int tid) {
; #pragma unroll
;     for (int i = 0; i < 8; ++i) { const int idx = tid + 512 * i, row = idx >> 6, c4 = idx & 63; LAS float* d = scr + row * 257 + 4 * c4; d[0] = v[i].x; d[1] = v[i].y; d[2] = v[i].z; d[3] = v[i].w; }
;     __syncthreads();
.LBB0_1811:
	v_add_u32_e32 v4, s26, v157
	v_add_u32_e32 v6, s26, v163
	v_add_u32_e32 v20, s26, v177
	v_add_u32_e32 v22, s26, v179
	v_add_u32_e32 v36, s26, v181
	v_add_u32_e32 v38, s26, v183
	v_add_u32_e32 v82, s26, v185
	v_add_u32_e32 v84, s26, v187
	v_mad_i64_i32 v[4:5], s[58:59], s34, v4, 0
	v_mad_i64_i32 v[6:7], s[58:59], s34, v6, 0
	v_mad_i64_i32 v[20:21], s[58:59], s34, v20, 0
	v_mad_i64_i32 v[22:23], s[58:59], s34, v22, 0
	v_mad_i64_i32 v[36:37], s[58:59], s34, v36, 0
	v_mad_i64_i32 v[38:39], s[58:59], s34, v38, 0
	v_mad_i64_i32 v[82:83], s[58:59], s34, v82, 0
	v_mad_i64_i32 v[84:85], s[34:35], s34, v84, 0
	v_lshl_add_u64 v[4:5], v[4:5], 2, s[30:31]
	s_lshl_b32 s44, s19, 2
	v_lshl_add_u64 v[6:7], v[6:7], 2, s[30:31]
	v_lshl_add_u64 v[20:21], v[20:21], 2, s[30:31]
	v_lshl_add_u64 v[22:23], v[22:23], 2, s[30:31]
	v_lshl_add_u64 v[36:37], v[36:37], 2, s[30:31]
	v_lshl_add_u64 v[38:39], v[38:39], 2, s[30:31]
	v_lshl_add_u64 v[82:83], v[82:83], 2, s[30:31]
	v_lshl_add_u64 v[84:85], v[84:85], 2, s[30:31]
	v_lshl_add_u64 v[4:5], v[4:5], 0, s[44:45]
	v_lshl_add_u64 v[6:7], v[6:7], 0, s[44:45]
	v_lshl_add_u64 v[20:21], v[20:21], 0, s[44:45]
	v_lshl_add_u64 v[22:23], v[22:23], 0, s[44:45]
	v_lshl_add_u64 v[36:37], v[36:37], 0, s[44:45]
	v_lshl_add_u64 v[38:39], v[38:39], 0, s[44:45]
	v_lshl_add_u64 v[82:83], v[82:83], 0, s[44:45]
	v_lshl_add_u64 v[84:85], v[84:85], 0, s[44:45]
	v_lshl_add_u64 v[4:5], v[4:5], 0, v[64:65]
	v_lshl_add_u64 v[6:7], v[6:7], 0, v[64:65]
	v_lshl_add_u64 v[20:21], v[20:21], 0, v[64:65]
	v_lshl_add_u64 v[22:23], v[22:23], 0, v[64:65]
	v_lshl_add_u64 v[36:37], v[36:37], 0, v[64:65]
	v_lshl_add_u64 v[38:39], v[38:39], 0, v[64:65]
	v_lshl_add_u64 v[82:83], v[82:83], 0, v[64:65]
	v_lshl_add_u64 v[84:85], v[84:85], 0, v[64:65]
	global_load_dwordx4 v[12:15], v[4:5], off nt
	s_nop 0
	global_load_dwordx4 v[4:7], v[6:7], off nt
	s_nop 0
	global_load_dwordx4 v[28:31], v[20:21], off nt
	s_nop 0
	global_load_dwordx4 v[20:23], v[22:23], off nt
	s_nop 0
	global_load_dwordx4 v[44:47], v[36:37], off nt
	s_nop 0
	global_load_dwordx4 v[36:39], v[38:39], off nt
	s_nop 0
	global_load_dwordx4 v[90:93], v[82:83], off nt
	s_nop 0
	global_load_dwordx4 v[82:85], v[84:85], off nt
	s_waitcnt vmcnt(23)
	ds_write2_b32 v236, v52, v53 offset1:1
	ds_write2_b32 v236, v54, v55 offset0:2 offset1:3
	s_waitcnt vmcnt(22)
	ds_write2_b32 v237, v48, v49 offset1:1
	ds_write2_b32 v237, v50, v51 offset0:2 offset1:3
	s_waitcnt vmcnt(21)
	ds_write2_b32 v238, v94, v95 offset1:1
	ds_write2_b32 v238, v96, v97 offset0:2 offset1:3
	s_waitcnt vmcnt(20)
	ds_write2_b32 v239, v56, v57 offset1:1
	ds_write2_b32 v239, v58, v59 offset0:2 offset1:3
	s_waitcnt vmcnt(19)
	ds_write2_b32 v240, v102, v103 offset1:1
	ds_write2_b32 v240, v104, v105 offset0:2 offset1:3
	s_waitcnt vmcnt(18)
	ds_write2_b32 v241, v98, v99 offset1:1
	ds_write2_b32 v241, v100, v101 offset0:2 offset1:3
	s_waitcnt vmcnt(17)
	ds_write2_b32 v242, v110, v111 offset1:1
	ds_write2_b32 v242, v112, v113 offset0:2 offset1:3
	s_waitcnt vmcnt(16)
	ds_write2_b32 v243, v106, v107 offset1:1
	ds_write2_b32 v243, v108, v109 offset0:2 offset1:3
	s_waitcnt lgkmcnt(0)
	s_barrier
; #define LAS __attribute__((address_space(3)))
; DI unsigned pk2(float lo, float hi) { f32x2 v = {lo, hi}; return __builtin_bit_cast(unsigned, __builtin_convertvector(v, bf16v2)); }
; DI ConvItem conv_item(int it, const float* wg, const float* wu, const float* wdn, bf16_t* we, bf16_t* wd) {
;     ConvItem c; const int e = it / 96; int r = it % 96;
;     if (r < 64) { const int up = r >> 5; r &= 31; c.src = (up ? wu : wg) + (size_t)e * DM * DEXP; c.ld = DEXP; c.k0 = (r >> 1) * 64; c.n0 = (r & 1) * 256; c.dst = we + (size_t)e * 1024 * 1024; c.Kd = 1024; c.mode = up; }
;     else { r -= 64; c.src = wdn + (size_t)e * DEXP * DM; c.ld = DM; c.k0 = (r >> 2) * 64; c.n0 = (r & 3) * 256; c.dst = wd + (size_t)e * 1024 * 512; c.Kd = 512; c.mode = 2; }
; DI void conv_store(const ConvItem& c, const f32x4 (&v)[8], LAS float* scr, int tid) {
;     ...
;     for (int i = 0; i < 4; ++i) { const int idx = tid + 512 * i, n = idx >> 3, cc = idx & 7; const LAS float* sp = scr + (8 * cc) * 257 + n;
;         u32x4 o; o.x = pk2(sp[0], sp[257]); o.y = pk2(sp[2 * 257], sp[3 * 257]); o.z = pk2(sp[4 * 257], sp[5 * 257]); o.w = pk2(sp[6 * 257], sp[7 * 257]);
;         const int h = c.n0 + n; const int drow = (c.mode == 2) ? h : ((h >> 7) * 256 + c.mode * 128 + (h & 127));
;         *(u32x4*)(c.dst + (size_t)drow * c.Kd + c.k0 + 8 * cc) = o; }
;     __syncthreads();
	ds_read_b32 v48, v188
	ds_read_b32 v49, v188 offset:1028
	ds_read_b32 v50, v188 offset:2056
	ds_read_b32 v51, v188 offset:3084
	ds_read_b32 v52, v188 offset:4112
	ds_read_b32 v53, v188 offset:5140
	ds_read_b32 v54, v188 offset:6168
	ds_read_b32 v55, v188 offset:7196
	s_cmp_eq_u32 s29, 2
	s_cselect_b64 vcc, -1, 0
	s_lshl_b32 s21, s29, 7
	s_waitcnt lgkmcnt(6)
	v_cvt_pk_bf16_f32 v48, v48, v49
	s_waitcnt lgkmcnt(4)
	v_cvt_pk_bf16_f32 v49, v50, v51
	s_waitcnt lgkmcnt(2)
	v_cvt_pk_bf16_f32 v50, v52, v53
	v_add_u32_e32 v52, s21, v190
	v_cndmask_b32_e32 v52, v52, v150, vcc
	v_mad_i64_i32 v[52:53], s[30:31], s20, v52, 0
	s_mov_b32 s29, s45
	v_lshl_add_u64 v[52:53], v[52:53], 1, s[4:5]
	s_lshl_b64 s[28:29], s[28:29], 1
	v_lshl_add_u64 v[52:53], v[52:53], 0, s[28:29]
	v_lshlrev_b32_e32 v164, 1, v148
	v_mov_b32_e32 v165, v65
	s_waitcnt lgkmcnt(0)
	v_cvt_pk_bf16_f32 v51, v54, v55
	v_lshl_add_u64 v[52:53], v[52:53], 0, v[164:165]
	ds_read_b32 v54, v191
	ds_read_b32 v55, v191 offset:1028
	ds_read_b32 v56, v191 offset:2056
	ds_read_b32 v57, v191 offset:3084
	ds_read_b32 v58, v191 offset:4112
	ds_read_b32 v59, v191 offset:5140
	ds_read_b32 v94, v191 offset:6168
	ds_read_b32 v95, v191 offset:7196
	global_store_dwordx4 v[52:53], v[48:51], off nt
	v_add_u32_e32 v52, s21, v193
	v_cndmask_b32_e32 v52, v52, v152, vcc
	v_mad_i64_i32 v[52:53], s[30:31], s20, v52, 0
	v_lshl_add_u64 v[52:53], v[52:53], 1, s[4:5]
	v_lshl_add_u64 v[52:53], v[52:53], 0, s[28:29]
	s_waitcnt lgkmcnt(6)
	v_cvt_pk_bf16_f32 v48, v54, v55
	s_waitcnt lgkmcnt(4)
	v_cvt_pk_bf16_f32 v49, v56, v57
	s_waitcnt lgkmcnt(2)
	v_cvt_pk_bf16_f32 v50, v58, v59
	s_waitcnt lgkmcnt(0)
	v_cvt_pk_bf16_f32 v51, v94, v95
	v_lshl_add_u64 v[52:53], v[52:53], 0, v[164:165]
	ds_read_b32 v54, v194
	ds_read_b32 v55, v194 offset:1028
	ds_read_b32 v56, v194 offset:2056
	ds_read_b32 v57, v194 offset:3084
	ds_read_b32 v58, v194 offset:4112
	ds_read_b32 v59, v194 offset:5140
	ds_read_b32 v94, v194 offset:6168
	ds_read_b32 v95, v194 offset:7196
	global_store_dwordx4 v[52:53], v[48:51], off nt
	v_add_u32_e32 v52, s21, v196
	v_cndmask_b32_e32 v52, v52, v154, vcc
	v_mad_i64_i32 v[52:53], s[30:31], s20, v52, 0
	v_lshl_add_u64 v[52:53], v[52:53], 1, s[4:5]
	v_lshl_add_u64 v[52:53], v[52:53], 0, s[28:29]
	s_waitcnt lgkmcnt(6)
	v_cvt_pk_bf16_f32 v48, v54, v55
	s_waitcnt lgkmcnt(4)
	v_cvt_pk_bf16_f32 v49, v56, v57
	s_waitcnt lgkmcnt(2)
	v_cvt_pk_bf16_f32 v50, v58, v59
	s_waitcnt lgkmcnt(0)
	v_cvt_pk_bf16_f32 v51, v94, v95
	v_lshl_add_u64 v[52:53], v[52:53], 0, v[164:165]
	ds_read_b32 v54, v197
	ds_read_b32 v55, v197 offset:1028
	ds_read_b32 v56, v197 offset:2056
	ds_read_b32 v57, v197 offset:3084
	ds_read_b32 v58, v197 offset:4112
	ds_read_b32 v59, v197 offset:5140
	ds_read_b32 v94, v197 offset:6168
	ds_read_b32 v95, v197 offset:7196
	global_store_dwordx4 v[52:53], v[48:51], off nt
	v_add_u32_e32 v52, s21, v199
	v_cndmask_b32_e32 v52, v52, v156, vcc
	v_mad_i64_i32 v[52:53], s[20:21], s20, v52, 0
	v_lshl_add_u64 v[52:53], v[52:53], 1, s[4:5]
	s_or_b32 s4, s56, 3
	s_mul_hi_i32 s5, s4, 0x2aaaaaab
	s_lshr_b32 s20, s5, 31
	s_ashr_i32 s5, s5, 4
	s_add_i32 s20, s5, s20
	s_mul_i32 s5, s20, 0x60
	v_lshl_add_u64 v[52:53], v[52:53], 0, s[28:29]
	s_sub_i32 s23, s4, s5
	s_waitcnt lgkmcnt(6)
	v_cvt_pk_bf16_f32 v48, v54, v55
	s_waitcnt lgkmcnt(4)
	v_cvt_pk_bf16_f32 v49, v56, v57
	s_waitcnt lgkmcnt(2)
	v_cvt_pk_bf16_f32 v50, v58, v59
	s_waitcnt lgkmcnt(0)
	v_cvt_pk_bf16_f32 v51, v94, v95
	v_lshl_add_u64 v[52:53], v[52:53], 0, v[164:165]
	s_cmp_lt_i32 s23, 64
	s_mov_b64 s[34:35], -1
	global_store_dwordx4 v[52:53], v[48:51], off nt
	s_barrier
	s_cbranch_scc1 .LBB0_1813
	s_ashr_i32 s21, s20, 31
	s_lshl_b64 s[4:5], s[20:21], 21
	s_add_u32 s30, s54, s4
	s_addc_u32 s31, s55, s5
	s_lshl_b32 s4, s23, 4
	s_add_i32 s4, s4, 0x7ffffc00
	s_and_b32 s28, s4, 0x7fffffc0
	s_lshl_b64 s[4:5], s[20:21], 20
	s_add_u32 s4, s77, s4
	s_addc_u32 s5, s78, s5
	s_mov_b64 s[34:35], 0

; #define LAS __attribute__((address_space(3)))
; DI unsigned pk2(float lo, float hi) { f32x2 v = {lo, hi}; return __builtin_bit_cast(unsigned, __builtin_convertvector(v, bf16v2)); }
; DI void conv_load(const ConvItem& c, f32x4 (&v)[8], int tid) {
; #pragma unroll
;     for (int i = 0; i < 8; ++i) { const int idx = tid + 512 * i, row = idx >> 6, c4 = idx & 63; v[i] = *(const f32x4*)(c.src + (size_t)(c.k0 + row) * c.ld + c.n0 + 4 * c4); }
; }
; DI void conv_store(const ConvItem& c, const f32x4 (&v)[8], LAS float* scr, int tid) {
; #pragma unroll
;     for (int i = 0; i < 8; ++i) { const int idx = tid + 512 * i, row = idx >> 6, c4 = idx & 63; LAS float* d = scr + row * 257 + 4 * c4; d[0] = v[i].x; d[1] = v[i].y; d[2] = v[i].z; d[3] = v[i].w; }
;     __syncthreads();
; #pragma unroll
;     for (int i = 0; i < 4; ++i) { const int idx = tid + 512 * i, n = idx >> 3, cc = idx & 7; const LAS float* sp = scr + (8 * cc) * 257 + n;
;         u32x4 o; o.x = pk2(sp[0], sp[257]); o.y = pk2(sp[2 * 257], sp[3 * 257]); o.z = pk2(sp[4 * 257], sp[5 * 257]); o.w = pk2(sp[6 * 257], sp[7 * 257]);
;         const int h = c.n0 + n; const int drow = (c.mode == 2) ? h : ((h >> 7) * 256 + c.mode * 128 + (h & 127));
;         *(u32x4*)(c.dst + (size_t)drow * c.Kd + c.k0 + 8 * cc) = o; }
;     __syncthreads();
.LBB0_1816:
	v_add_u32_e32 v48, s28, v157
	v_add_u32_e32 v50, s28, v163
	v_add_u32_e32 v56, s28, v177
	v_add_u32_e32 v58, s28, v179
	v_add_u32_e32 v98, s28, v181
	v_add_u32_e32 v100, s28, v183
	v_add_u32_e32 v106, s28, v185
	v_add_u32_e32 v108, s28, v187
	v_mad_i64_i32 v[48:49], s[58:59], s34, v48, 0
	v_mad_i64_i32 v[50:51], s[58:59], s34, v50, 0
	v_mad_i64_i32 v[56:57], s[58:59], s34, v56, 0
	v_mad_i64_i32 v[58:59], s[58:59], s34, v58, 0
	v_mad_i64_i32 v[98:99], s[58:59], s34, v98, 0
	v_mad_i64_i32 v[100:101], s[58:59], s34, v100, 0
	v_mad_i64_i32 v[106:107], s[58:59], s34, v106, 0
	v_mad_i64_i32 v[108:109], s[34:35], s34, v108, 0
	v_lshl_add_u64 v[48:49], v[48:49], 2, s[30:31]
	s_lshl_b32 s44, s21, 2
	v_lshl_add_u64 v[50:51], v[50:51], 2, s[30:31]
	v_lshl_add_u64 v[56:57], v[56:57], 2, s[30:31]
	v_lshl_add_u64 v[58:59], v[58:59], 2, s[30:31]
	v_lshl_add_u64 v[98:99], v[98:99], 2, s[30:31]
	v_lshl_add_u64 v[100:101], v[100:101], 2, s[30:31]
	v_lshl_add_u64 v[106:107], v[106:107], 2, s[30:31]
	v_lshl_add_u64 v[108:109], v[108:109], 2, s[30:31]
	v_lshl_add_u64 v[48:49], v[48:49], 0, s[44:45]
	v_lshl_add_u64 v[50:51], v[50:51], 0, s[44:45]
	v_lshl_add_u64 v[56:57], v[56:57], 0, s[44:45]
	v_lshl_add_u64 v[58:59], v[58:59], 0, s[44:45]
	v_lshl_add_u64 v[98:99], v[98:99], 0, s[44:45]
	v_lshl_add_u64 v[100:101], v[100:101], 0, s[44:45]
	v_lshl_add_u64 v[106:107], v[106:107], 0, s[44:45]
	v_lshl_add_u64 v[108:109], v[108:109], 0, s[44:45]
	v_lshl_add_u64 v[48:49], v[48:49], 0, v[64:65]
	v_lshl_add_u64 v[50:51], v[50:51], 0, v[64:65]
	v_lshl_add_u64 v[56:57], v[56:57], 0, v[64:65]
	v_lshl_add_u64 v[58:59], v[58:59], 0, v[64:65]
	v_lshl_add_u64 v[98:99], v[98:99], 0, v[64:65]
	v_lshl_add_u64 v[100:101], v[100:101], 0, v[64:65]
	v_lshl_add_u64 v[106:107], v[106:107], 0, v[64:65]
	v_lshl_add_u64 v[108:109], v[108:109], 0, v[64:65]
	global_load_dwordx4 v[52:55], v[48:49], off nt
	s_nop 0
	global_load_dwordx4 v[48:51], v[50:51], off nt
	s_nop 0
	global_load_dwordx4 v[94:97], v[56:57], off nt
	s_nop 0
	global_load_dwordx4 v[56:59], v[58:59], off nt
	s_nop 0
	global_load_dwordx4 v[102:105], v[98:99], off nt
	s_nop 0
	global_load_dwordx4 v[98:101], v[100:101], off nt
	s_nop 0
	global_load_dwordx4 v[110:113], v[106:107], off nt
	s_nop 0
	global_load_dwordx4 v[106:109], v[108:109], off nt
	s_waitcnt vmcnt(27)
	ds_write2_b32 v236, v8, v9 offset1:1
	ds_write2_b32 v236, v10, v11 offset0:2 offset1:3
	s_waitcnt vmcnt(26)
	ds_write2_b32 v237, v0, v1 offset1:1
	ds_write2_b32 v237, v2, v3 offset0:2 offset1:3
	s_waitcnt vmcnt(25)
	ds_write2_b32 v238, v24, v25 offset1:1
	ds_write2_b32 v238, v26, v27 offset0:2 offset1:3
	s_waitcnt vmcnt(24)
	ds_write2_b32 v239, v16, v17 offset1:1
	ds_write2_b32 v239, v18, v19 offset0:2 offset1:3
	s_waitcnt vmcnt(23)
	ds_write2_b32 v240, v40, v41 offset1:1
	ds_write2_b32 v240, v42, v43 offset0:2 offset1:3
	s_waitcnt vmcnt(22)
	ds_write2_b32 v241, v32, v33 offset1:1
	ds_write2_b32 v241, v34, v35 offset0:2 offset1:3
	s_waitcnt vmcnt(21)
	ds_write2_b32 v242, v86, v87 offset1:1
	ds_write2_b32 v242, v88, v89 offset0:2 offset1:3
	s_waitcnt vmcnt(20)
	ds_write2_b32 v243, v60, v61 offset1:1
	ds_write2_b32 v243, v62, v63 offset0:2 offset1:3
	s_waitcnt lgkmcnt(0)
	s_barrier
	ds_read_b32 v0, v188
	ds_read_b32 v1, v188 offset:1028
	ds_read_b32 v2, v188 offset:2056
	ds_read_b32 v3, v188 offset:3084
	ds_read_b32 v8, v188 offset:4112
	ds_read_b32 v9, v188 offset:5140
	ds_read_b32 v10, v188 offset:6168
	ds_read_b32 v11, v188 offset:7196
	s_cmp_eq_u32 s25, 2
	s_cselect_b64 vcc, -1, 0
	s_lshl_b32 s23, s25, 7
	s_waitcnt lgkmcnt(6)
	v_cvt_pk_bf16_f32 v0, v0, v1
	s_waitcnt lgkmcnt(4)
	v_cvt_pk_bf16_f32 v1, v2, v3
	s_waitcnt lgkmcnt(2)
	v_cvt_pk_bf16_f32 v2, v8, v9
	v_add_u32_e32 v8, s23, v201
	v_cndmask_b32_e32 v8, v8, v200, vcc
	v_mad_i64_i32 v[8:9], s[30:31], s22, v8, 0
	s_mov_b32 s25, s45
	v_lshl_add_u64 v[8:9], v[8:9], 1, s[6:7]
	s_lshl_b64 s[24:25], s[24:25], 1
	v_lshl_add_u64 v[8:9], v[8:9], 0, s[24:25]
	v_mov_b32_e32 v165, v65
	s_waitcnt lgkmcnt(0)
	v_cvt_pk_bf16_f32 v3, v10, v11
	v_lshl_add_u64 v[8:9], v[8:9], 0, v[164:165]
	ds_read_b32 v10, v191
	ds_read_b32 v11, v191 offset:1028
	ds_read_b32 v16, v191 offset:2056
	ds_read_b32 v17, v191 offset:3084
	ds_read_b32 v18, v191 offset:4112
	ds_read_b32 v19, v191 offset:5140
	ds_read_b32 v24, v191 offset:6168
	ds_read_b32 v25, v191 offset:7196
	global_store_dwordx4 v[8:9], v[0:3], off nt
	v_add_u32_e32 v8, s23, v207
	v_cndmask_b32_e32 v8, v8, v206, vcc
	v_mad_i64_i32 v[8:9], s[30:31], s22, v8, 0
	v_lshl_add_u64 v[8:9], v[8:9], 1, s[6:7]
	v_lshl_add_u64 v[8:9], v[8:9], 0, s[24:25]
	s_waitcnt lgkmcnt(6)
	v_cvt_pk_bf16_f32 v0, v10, v11
	s_waitcnt lgkmcnt(4)
	v_cvt_pk_bf16_f32 v1, v16, v17
	s_waitcnt lgkmcnt(2)
	v_cvt_pk_bf16_f32 v2, v18, v19
	s_waitcnt lgkmcnt(0)
	v_cvt_pk_bf16_f32 v3, v24, v25
	v_lshl_add_u64 v[8:9], v[8:9], 0, v[164:165]
	ds_read_b32 v10, v194
	ds_read_b32 v11, v194 offset:1028
	ds_read_b32 v16, v194 offset:2056
	ds_read_b32 v17, v194 offset:3084
	ds_read_b32 v18, v194 offset:4112
	ds_read_b32 v19, v194 offset:5140
	ds_read_b32 v24, v194 offset:6168
	ds_read_b32 v25, v194 offset:7196
	global_store_dwordx4 v[8:9], v[0:3], off nt
	v_add_u32_e32 v8, s23, v209
	v_cndmask_b32_e32 v8, v8, v208, vcc
	v_mad_i64_i32 v[8:9], s[30:31], s22, v8, 0
	v_lshl_add_u64 v[8:9], v[8:9], 1, s[6:7]
	v_lshl_add_u64 v[8:9], v[8:9], 0, s[24:25]
	s_waitcnt lgkmcnt(6)
	v_cvt_pk_bf16_f32 v0, v10, v11
	s_waitcnt lgkmcnt(4)
	v_cvt_pk_bf16_f32 v1, v16, v17
	s_waitcnt lgkmcnt(2)
	v_cvt_pk_bf16_f32 v2, v18, v19
	s_waitcnt lgkmcnt(0)
	v_cvt_pk_bf16_f32 v3, v24, v25
	v_lshl_add_u64 v[8:9], v[8:9], 0, v[164:165]
	ds_read_b32 v10, v197
	ds_read_b32 v11, v197 offset:1028
	ds_read_b32 v16, v197 offset:2056
	ds_read_b32 v17, v197 offset:3084
	ds_read_b32 v18, v197 offset:4112
	ds_read_b32 v19, v197 offset:5140
	ds_read_b32 v24, v197 offset:6168
	ds_read_b32 v25, v197 offset:7196
	global_store_dwordx4 v[8:9], v[0:3], off nt
	v_add_u32_e32 v8, s23, v211
	v_cndmask_b32_e32 v8, v8, v210, vcc
	v_mad_i64_i32 v[8:9], s[22:23], s22, v8, 0
	v_lshl_add_u64 v[8:9], v[8:9], 1, s[6:7]
	s_add_i32 s6, s56, 4
	s_mul_hi_i32 s7, s6, 0x2aaaaaab
	s_lshr_b32 s22, s7, 31
	s_ashr_i32 s7, s7, 4
	s_add_i32 s22, s7, s22
	s_mul_i32 s7, s22, 0x60
	v_lshl_add_u64 v[8:9], v[8:9], 0, s[24:25]
	s_sub_i32 s44, s6, s7
	s_waitcnt lgkmcnt(6)
	v_cvt_pk_bf16_f32 v0, v10, v11
	s_waitcnt lgkmcnt(4)
	v_cvt_pk_bf16_f32 v1, v16, v17
	s_waitcnt lgkmcnt(2)
	v_cvt_pk_bf16_f32 v2, v18, v19
	s_waitcnt lgkmcnt(0)
	v_cvt_pk_bf16_f32 v3, v24, v25
	v_lshl_add_u64 v[8:9], v[8:9], 0, v[164:165]
	s_cmp_lt_i32 s44, 64
	s_mov_b64 s[34:35], -1
	global_store_dwordx4 v[8:9], v[0:3], off nt
	s_barrier
	s_cbranch_scc1 .LBB0_1818
	s_ashr_i32 s23, s22, 31
	s_lshl_b64 s[6:7], s[22:23], 21
	s_add_u32 s30, s54, s6
	s_addc_u32 s31, s55, s7
	s_lshl_b32 s6, s44, 4
	s_add_i32 s6, s6, 0x7ffffc00
	s_and_b32 s24, s6, 0x7fffffc0
	s_lshl_b64 s[6:7], s[22:23], 20
	s_add_u32 s6, s77, s6
	s_addc_u32 s7, s78, s7
	s_mov_b64 s[34:35], 0

; #define LAS __attribute__((address_space(3)))
; DI void conv_load(const ConvItem& c, f32x4 (&v)[8], int tid) {
; #pragma unroll
;     for (int i = 0; i < 8; ++i) { const int idx = tid + 512 * i, row = idx >> 6, c4 = idx & 63; v[i] = *(const f32x4*)(c.src + (size_t)(c.k0 + row) * c.ld + c.n0 + 4 * c4); }
; }
; DI void conv_store(const ConvItem& c, const f32x4 (&v)[8], LAS float* scr, int tid) {
; #pragma unroll
;     for (int i = 0; i < 8; ++i) { const int idx = tid + 512 * i, row = idx >> 6, c4 = idx & 63; LAS float* d = scr + row * 257 + 4 * c4; d[0] = v[i].x; d[1] = v[i].y; d[2] = v[i].z; d[3] = v[i].w; }
;     __syncthreads();
.LBB0_1821:
	v_add_u32_e32 v0, s24, v157
	v_add_u32_e32 v2, s24, v163
	v_add_u32_e32 v16, s24, v177
	v_add_u32_e32 v18, s24, v179
	v_add_u32_e32 v32, s24, v181
	v_add_u32_e32 v34, s24, v183
	v_add_u32_e32 v60, s24, v185
	v_add_u32_e32 v62, s24, v187
	v_mad_i64_i32 v[0:1], s[58:59], s34, v0, 0
	v_mad_i64_i32 v[2:3], s[58:59], s34, v2, 0
	v_mad_i64_i32 v[16:17], s[58:59], s34, v16, 0
	v_mad_i64_i32 v[18:19], s[58:59], s34, v18, 0
	v_mad_i64_i32 v[32:33], s[58:59], s34, v32, 0
	v_mad_i64_i32 v[34:35], s[58:59], s34, v34, 0
	v_mad_i64_i32 v[60:61], s[58:59], s34, v60, 0
	v_mad_i64_i32 v[62:63], s[34:35], s34, v62, 0
	v_lshl_add_u64 v[0:1], v[0:1], 2, s[30:31]
	v_lshl_add_u64 v[2:3], v[2:3], 2, s[30:31]
	v_lshl_add_u64 v[16:17], v[16:17], 2, s[30:31]
	v_lshl_add_u64 v[18:19], v[18:19], 2, s[30:31]
	v_lshl_add_u64 v[32:33], v[32:33], 2, s[30:31]
	v_lshl_add_u64 v[34:35], v[34:35], 2, s[30:31]
	v_lshl_add_u64 v[60:61], v[60:61], 2, s[30:31]
	v_lshl_add_u64 v[62:63], v[62:63], 2, s[30:31]
	v_lshl_add_u64 v[0:1], v[0:1], 0, v[64:65]
	v_lshl_add_u64 v[2:3], v[2:3], 0, v[64:65]
	v_lshl_add_u64 v[16:17], v[16:17], 0, v[64:65]
	v_lshl_add_u64 v[18:19], v[18:19], 0, v[64:65]
	v_lshl_add_u64 v[32:33], v[32:33], 0, v[64:65]
	v_lshl_add_u64 v[34:35], v[34:35], 0, v[64:65]
	v_lshl_add_u64 v[60:61], v[60:61], 0, v[64:65]
	v_lshl_add_u64 v[62:63], v[62:63], 0, v[64:65]
	global_load_dwordx4 v[8:11], v[0:1], off nt
	s_nop 0
	global_load_dwordx4 v[0:3], v[2:3], off nt
	s_nop 0
	global_load_dwordx4 v[24:27], v[16:17], off nt
	s_nop 0
	global_load_dwordx4 v[16:19], v[18:19], off nt
	s_nop 0
	global_load_dwordx4 v[40:43], v[32:33], off nt
	s_nop 0
	global_load_dwordx4 v[32:35], v[34:35], off nt
	s_nop 0
	global_load_dwordx4 v[86:89], v[60:61], off nt
	s_nop 0
	global_load_dwordx4 v[60:63], v[62:63], off nt
	s_waitcnt vmcnt(31)
	ds_write2_b32 v236, v12, v13 offset1:1
	ds_write2_b32 v236, v14, v15 offset0:2 offset1:3
	s_waitcnt vmcnt(30)
	ds_write2_b32 v237, v4, v5 offset1:1
	ds_write2_b32 v237, v6, v7 offset0:2 offset1:3
	s_waitcnt vmcnt(29)
	ds_write2_b32 v238, v28, v29 offset1:1
	ds_write2_b32 v238, v30, v31 offset0:2 offset1:3
	s_waitcnt vmcnt(28)
	ds_write2_b32 v239, v20, v21 offset1:1
	ds_write2_b32 v239, v22, v23 offset0:2 offset1:3
	s_waitcnt vmcnt(27)
	ds_write2_b32 v240, v44, v45 offset1:1
	ds_write2_b32 v240, v46, v47 offset0:2 offset1:3
	s_waitcnt vmcnt(26)
	ds_write2_b32 v241, v36, v37 offset1:1
	ds_write2_b32 v241, v38, v39 offset0:2 offset1:3
	s_waitcnt vmcnt(25)
	ds_write2_b32 v242, v90, v91 offset1:1
	ds_write2_b32 v242, v92, v93 offset0:2 offset1:3
	s_waitcnt vmcnt(24)
	ds_write2_b32 v243, v82, v83 offset1:1
	ds_write2_b32 v243, v84, v85 offset0:2 offset1:3
	s_waitcnt lgkmcnt(0)
	s_barrier
; #define LAS __attribute__((address_space(3)))
; DI unsigned pk2(float lo, float hi) { f32x2 v = {lo, hi}; return __builtin_bit_cast(unsigned, __builtin_convertvector(v, bf16v2)); }
; DI ConvItem conv_item(int it, const float* wg, const float* wu, const float* wdn, bf16_t* we, bf16_t* wd) {
;     ConvItem c; const int e = it / 96; int r = it % 96;
;     if (r < 64) { const int up = r >> 5; r &= 31; c.src = (up ? wu : wg) + (size_t)e * DM * DEXP; c.ld = DEXP; c.k0 = (r >> 1) * 64; c.n0 = (r & 1) * 256; c.dst = we + (size_t)e * 1024 * 1024; c.Kd = 1024; c.mode = up; }
;     else { r -= 64; c.src = wdn + (size_t)e * DEXP * DM; c.ld = DM; c.k0 = (r >> 2) * 64; c.n0 = (r & 3) * 256; c.dst = wd + (size_t)e * 1024 * 512; c.Kd = 512; c.mode = 2; }
; DI void conv_store(const ConvItem& c, const f32x4 (&v)[8], LAS float* scr, int tid) {
;     ...
;     for (int i = 0; i < 4; ++i) { const int idx = tid + 512 * i, n = idx >> 3, cc = idx & 7; const LAS float* sp = scr + (8 * cc) * 257 + n;
;         u32x4 o; o.x = pk2(sp[0], sp[257]); o.y = pk2(sp[2 * 257], sp[3 * 257]); o.z = pk2(sp[4 * 257], sp[5 * 257]); o.w = pk2(sp[6 * 257], sp[7 * 257]);
;         const int h = c.n0 + n; const int drow = (c.mode == 2) ? h : ((h >> 7) * 256 + c.mode * 128 + (h & 127));
;         *(u32x4*)(c.dst + (size_t)drow * c.Kd + c.k0 + 8 * cc) = o; }
;     __syncthreads();
	ds_read_b32 v4, v188
	ds_read_b32 v5, v188 offset:1028
	ds_read_b32 v6, v188 offset:2056
	ds_read_b32 v7, v188 offset:3084
	ds_read_b32 v12, v188 offset:4112
	ds_read_b32 v13, v188 offset:5140
	ds_read_b32 v14, v188 offset:6168
	ds_read_b32 v15, v188 offset:7196
	s_waitcnt lgkmcnt(6)
	v_cvt_pk_bf16_f32 v4, v4, v5
	s_waitcnt lgkmcnt(4)
	v_cvt_pk_bf16_f32 v5, v6, v7
	s_waitcnt lgkmcnt(2)
	v_cvt_pk_bf16_f32 v6, v12, v13
	v_add_u32_e32 v12, s19, v150
	s_cmp_eq_u32 s27, 2
	v_lshlrev_b32_e32 v13, 1, v12
	s_cselect_b64 vcc, -1, 0
	v_and_b32_e32 v13, 0xffffff00, v13
	s_lshl_b32 s23, s27, 7
	v_add_u32_e32 v13, s23, v13
	v_or_b32_e32 v13, v13, v189
	v_cndmask_b32_e32 v12, v13, v12, vcc
	v_mad_i64_i32 v[12:13], s[30:31], s18, v12, 0
	s_mov_b32 s27, s45
	v_lshl_add_u64 v[12:13], v[12:13], 1, s[2:3]
	s_lshl_b64 s[26:27], s[26:27], 1
	v_lshl_add_u64 v[12:13], v[12:13], 0, s[26:27]
	v_mov_b32_e32 v165, v65
	s_waitcnt lgkmcnt(0)
	v_cvt_pk_bf16_f32 v7, v14, v15
	v_lshl_add_u64 v[12:13], v[12:13], 0, v[164:165]
	ds_read_b32 v14, v191
	ds_read_b32 v15, v191 offset:1028
	ds_read_b32 v20, v191 offset:2056
	ds_read_b32 v21, v191 offset:3084
	ds_read_b32 v22, v191 offset:4112
	ds_read_b32 v23, v191 offset:5140
	ds_read_b32 v28, v191 offset:6168
	ds_read_b32 v29, v191 offset:7196
	global_store_dwordx4 v[12:13], v[4:7], off nt
	v_add_u32_e32 v12, s19, v152
	v_lshlrev_b32_e32 v13, 1, v12
	v_and_b32_e32 v13, 0xffffff00, v13
	v_add_u32_e32 v13, s23, v13
	v_or_b32_e32 v13, v13, v192
	v_cndmask_b32_e32 v12, v13, v12, vcc
	v_mad_i64_i32 v[12:13], s[30:31], s18, v12, 0
	v_lshl_add_u64 v[12:13], v[12:13], 1, s[2:3]
	v_lshl_add_u64 v[12:13], v[12:13], 0, s[26:27]
	s_waitcnt lgkmcnt(6)
	v_cvt_pk_bf16_f32 v4, v14, v15
	s_waitcnt lgkmcnt(4)
	v_cvt_pk_bf16_f32 v5, v20, v21
	s_waitcnt lgkmcnt(2)
	v_cvt_pk_bf16_f32 v6, v22, v23
	s_waitcnt lgkmcnt(0)
	v_cvt_pk_bf16_f32 v7, v28, v29
	v_lshl_add_u64 v[12:13], v[12:13], 0, v[164:165]
	ds_read_b32 v14, v194
	ds_read_b32 v15, v194 offset:1028
	ds_read_b32 v20, v194 offset:2056
	ds_read_b32 v21, v194 offset:3084
	ds_read_b32 v22, v194 offset:4112
	ds_read_b32 v23, v194 offset:5140
	ds_read_b32 v28, v194 offset:6168
	ds_read_b32 v29, v194 offset:7196
	global_store_dwordx4 v[12:13], v[4:7], off nt
	v_add_u32_e32 v12, s19, v154
	v_lshlrev_b32_e32 v13, 1, v12
	v_and_b32_e32 v13, 0xffffff00, v13
	v_add_u32_e32 v13, s23, v13
	v_or_b32_e32 v13, v13, v195
	v_cndmask_b32_e32 v12, v13, v12, vcc
	v_mad_i64_i32 v[12:13], s[30:31], s18, v12, 0
	v_lshl_add_u64 v[12:13], v[12:13], 1, s[2:3]
	v_lshl_add_u64 v[12:13], v[12:13], 0, s[26:27]
	s_waitcnt lgkmcnt(6)
	v_cvt_pk_bf16_f32 v4, v14, v15
	s_waitcnt lgkmcnt(4)
	v_cvt_pk_bf16_f32 v5, v20, v21
	s_waitcnt lgkmcnt(2)
	v_cvt_pk_bf16_f32 v6, v22, v23
	s_waitcnt lgkmcnt(0)
	v_cvt_pk_bf16_f32 v7, v28, v29
	v_lshl_add_u64 v[12:13], v[12:13], 0, v[164:165]
	ds_read_b32 v14, v197
	ds_read_b32 v15, v197 offset:1028
	ds_read_b32 v20, v197 offset:2056
	ds_read_b32 v21, v197 offset:3084
	ds_read_b32 v22, v197 offset:4112
	ds_read_b32 v23, v197 offset:5140
	ds_read_b32 v28, v197 offset:6168
	ds_read_b32 v29, v197 offset:7196
	global_store_dwordx4 v[12:13], v[4:7], off nt
	v_add_u32_e32 v12, s19, v156
	v_lshlrev_b32_e32 v13, 1, v12
	v_and_b32_e32 v13, 0xffffff00, v13
	v_add_u32_e32 v13, s23, v13
	v_or_b32_e32 v13, v13, v198
	v_cndmask_b32_e32 v12, v13, v12, vcc
	v_mad_i64_i32 v[12:13], s[18:19], s18, v12, 0
	v_lshl_add_u64 v[12:13], v[12:13], 1, s[2:3]
	s_add_i32 s2, s56, 5
	s_mul_hi_i32 s3, s2, 0x2aaaaaab
	s_lshr_b32 s18, s3, 31
	s_ashr_i32 s3, s3, 4
	s_add_i32 s18, s3, s18
	s_mul_i32 s3, s18, 0x60
	v_lshl_add_u64 v[12:13], v[12:13], 0, s[26:27]
	s_sub_i32 s23, s2, s3
	s_waitcnt lgkmcnt(6)
	v_cvt_pk_bf16_f32 v4, v14, v15
	s_waitcnt lgkmcnt(4)
	v_cvt_pk_bf16_f32 v5, v20, v21
	s_waitcnt lgkmcnt(2)
	v_cvt_pk_bf16_f32 v6, v22, v23
	s_waitcnt lgkmcnt(0)
	v_cvt_pk_bf16_f32 v7, v28, v29
	v_lshl_add_u64 v[12:13], v[12:13], 0, v[164:165]
	s_cmp_lt_i32 s23, 64
	s_mov_b64 s[34:35], -1
	global_store_dwordx4 v[12:13], v[4:7], off nt
	s_barrier
	s_cbranch_scc1 .LBB0_1823
	s_ashr_i32 s19, s18, 31
	s_lshl_b64 s[2:3], s[18:19], 21
	s_add_u32 s30, s54, s2
	s_addc_u32 s31, s55, s3
	s_lshl_b32 s2, s23, 4
	s_add_i32 s2, s2, 0x7ffffc00
	s_and_b32 s26, s2, 0x7fffffc0
	s_lshl_b64 s[2:3], s[18:19], 20
	s_add_u32 s2, s77, s2
	s_addc_u32 s3, s78, s3
	s_mov_b64 s[34:35], 0

; #define LAS __attribute__((address_space(3)))
; DI void conv_load(const ConvItem& c, f32x4 (&v)[8], int tid) {
; #pragma unroll
;     for (int i = 0; i < 8; ++i) { const int idx = tid + 512 * i, row = idx >> 6, c4 = idx & 63; v[i] = *(const f32x4*)(c.src + (size_t)(c.k0 + row) * c.ld + c.n0 + 4 * c4); }
; }
; DI void conv_store(const ConvItem& c, const f32x4 (&v)[8], LAS float* scr, int tid) {
; #pragma unroll
;     for (int i = 0; i < 8; ++i) { const int idx = tid + 512 * i, row = idx >> 6, c4 = idx & 63; LAS float* d = scr + row * 257 + 4 * c4; d[0] = v[i].x; d[1] = v[i].y; d[2] = v[i].z; d[3] = v[i].w; }
;     __syncthreads();
.LBB0_1826:
	v_add_u32_e32 v4, s26, v157
	v_add_u32_e32 v6, s26, v163
	v_add_u32_e32 v20, s26, v177
	v_add_u32_e32 v22, s26, v179
	v_add_u32_e32 v36, s26, v181
	v_add_u32_e32 v38, s26, v183
	v_add_u32_e32 v82, s26, v185
	v_add_u32_e32 v84, s26, v187
	v_mad_i64_i32 v[4:5], s[58:59], s34, v4, 0
	v_mad_i64_i32 v[6:7], s[58:59], s34, v6, 0
	v_mad_i64_i32 v[20:21], s[58:59], s34, v20, 0
	v_mad_i64_i32 v[22:23], s[58:59], s34, v22, 0
	v_mad_i64_i32 v[36:37], s[58:59], s34, v36, 0
	v_mad_i64_i32 v[38:39], s[58:59], s34, v38, 0
	v_mad_i64_i32 v[82:83], s[58:59], s34, v82, 0
	v_mad_i64_i32 v[84:85], s[34:35], s34, v84, 0
	v_lshl_add_u64 v[4:5], v[4:5], 2, s[30:31]
	v_lshl_add_u64 v[6:7], v[6:7], 2, s[30:31]
	v_lshl_add_u64 v[20:21], v[20:21], 2, s[30:31]
	v_lshl_add_u64 v[22:23], v[22:23], 2, s[30:31]
	v_lshl_add_u64 v[36:37], v[36:37], 2, s[30:31]
	v_lshl_add_u64 v[38:39], v[38:39], 2, s[30:31]
	v_lshl_add_u64 v[82:83], v[82:83], 2, s[30:31]
	v_lshl_add_u64 v[84:85], v[84:85], 2, s[30:31]
	v_lshl_add_u64 v[4:5], v[4:5], 0, v[64:65]
	v_lshl_add_u64 v[6:7], v[6:7], 0, v[64:65]
	v_lshl_add_u64 v[20:21], v[20:21], 0, v[64:65]
	v_lshl_add_u64 v[22:23], v[22:23], 0, v[64:65]
	v_lshl_add_u64 v[36:37], v[36:37], 0, v[64:65]
	v_lshl_add_u64 v[38:39], v[38:39], 0, v[64:65]
	v_lshl_add_u64 v[82:83], v[82:83], 0, v[64:65]
	v_lshl_add_u64 v[84:85], v[84:85], 0, v[64:65]
	global_load_dwordx4 v[12:15], v[4:5], off offset:1024 nt
	s_nop 0
	global_load_dwordx4 v[4:7], v[6:7], off offset:1024 nt
	s_nop 0
	global_load_dwordx4 v[28:31], v[20:21], off offset:1024 nt
	s_nop 0
	global_load_dwordx4 v[20:23], v[22:23], off offset:1024 nt
	s_nop 0
	global_load_dwordx4 v[44:47], v[36:37], off offset:1024 nt
	s_nop 0
	global_load_dwordx4 v[36:39], v[38:39], off offset:1024 nt
	s_nop 0
	global_load_dwordx4 v[90:93], v[82:83], off offset:1024 nt
	s_nop 0
	global_load_dwordx4 v[82:85], v[84:85], off offset:1024 nt
	s_waitcnt vmcnt(31)
	ds_write2_b32 v236, v52, v53 offset1:1
	ds_write2_b32 v236, v54, v55 offset0:2 offset1:3
	s_waitcnt vmcnt(30)
	ds_write2_b32 v237, v48, v49 offset1:1
	ds_write2_b32 v237, v50, v51 offset0:2 offset1:3
	s_waitcnt vmcnt(29)
	ds_write2_b32 v238, v94, v95 offset1:1
	ds_write2_b32 v238, v96, v97 offset0:2 offset1:3
	s_waitcnt vmcnt(28)
	ds_write2_b32 v239, v56, v57 offset1:1
	ds_write2_b32 v239, v58, v59 offset0:2 offset1:3
	s_waitcnt vmcnt(27)
	ds_write2_b32 v240, v102, v103 offset1:1
	ds_write2_b32 v240, v104, v105 offset0:2 offset1:3
	s_waitcnt vmcnt(26)
	ds_write2_b32 v241, v98, v99 offset1:1
	ds_write2_b32 v241, v100, v101 offset0:2 offset1:3
	s_waitcnt vmcnt(25)
	ds_write2_b32 v242, v110, v111 offset1:1
	ds_write2_b32 v242, v112, v113 offset0:2 offset1:3
	s_waitcnt vmcnt(24)
	ds_write2_b32 v243, v106, v107 offset1:1
	ds_write2_b32 v243, v108, v109 offset0:2 offset1:3
	s_waitcnt lgkmcnt(0)
	s_barrier
; #define LAS __attribute__((address_space(3)))
; DI unsigned pk2(float lo, float hi) { f32x2 v = {lo, hi}; return __builtin_bit_cast(unsigned, __builtin_convertvector(v, bf16v2)); }
; DI ConvItem conv_item(int it, const float* wg, const float* wu, const float* wdn, bf16_t* we, bf16_t* wd) {
;     ConvItem c; const int e = it / 96; int r = it % 96;
;     if (r < 64) { const int up = r >> 5; r &= 31; c.src = (up ? wu : wg) + (size_t)e * DM * DEXP; c.ld = DEXP; c.k0 = (r >> 1) * 64; c.n0 = (r & 1) * 256; c.dst = we + (size_t)e * 1024 * 1024; c.Kd = 1024; c.mode = up; }
;     else { r -= 64; c.src = wdn + (size_t)e * DEXP * DM; c.ld = DM; c.k0 = (r >> 2) * 64; c.n0 = (r & 3) * 256; c.dst = wd + (size_t)e * 1024 * 512; c.Kd = 512; c.mode = 2; }
; DI void conv_store(const ConvItem& c, const f32x4 (&v)[8], LAS float* scr, int tid) {
;     ...
;     for (int i = 0; i < 4; ++i) { const int idx = tid + 512 * i, n = idx >> 3, cc = idx & 7; const LAS float* sp = scr + (8 * cc) * 257 + n;
;         u32x4 o; o.x = pk2(sp[0], sp[257]); o.y = pk2(sp[2 * 257], sp[3 * 257]); o.z = pk2(sp[4 * 257], sp[5 * 257]); o.w = pk2(sp[6 * 257], sp[7 * 257]);
;         const int h = c.n0 + n; const int drow = (c.mode == 2) ? h : ((h >> 7) * 256 + c.mode * 128 + (h & 127));
;         *(u32x4*)(c.dst + (size_t)drow * c.Kd + c.k0 + 8 * cc) = o; }
;     __syncthreads();
	ds_read_b32 v48, v188
	ds_read_b32 v49, v188 offset:1028
	ds_read_b32 v50, v188 offset:2056
	ds_read_b32 v51, v188 offset:3084
	ds_read_b32 v52, v188 offset:4112
	ds_read_b32 v53, v188 offset:5140
	ds_read_b32 v54, v188 offset:6168
	ds_read_b32 v55, v188 offset:7196
	s_waitcnt lgkmcnt(6)
	v_cvt_pk_bf16_f32 v48, v48, v49
	s_waitcnt lgkmcnt(4)
	v_cvt_pk_bf16_f32 v49, v50, v51
	s_waitcnt lgkmcnt(2)
	v_cvt_pk_bf16_f32 v50, v52, v53
	v_add_u32_e32 v52, s21, v150
	s_cmp_eq_u32 s29, 2
	v_lshlrev_b32_e32 v53, 1, v52
	s_cselect_b64 vcc, -1, 0
	v_and_b32_e32 v53, 0xffffff00, v53
	s_lshl_b32 s19, s29, 7
	v_add_u32_e32 v53, s19, v53
	v_or_b32_e32 v53, v53, v189
	v_cndmask_b32_e32 v52, v53, v52, vcc
	v_mad_i64_i32 v[52:53], s[30:31], s20, v52, 0
	s_mov_b32 s29, s45
	v_lshl_add_u64 v[52:53], v[52:53], 1, s[4:5]
	s_lshl_b64 s[28:29], s[28:29], 1
	v_lshl_add_u64 v[52:53], v[52:53], 0, s[28:29]
	v_mov_b32_e32 v165, v65
	s_waitcnt lgkmcnt(0)
	v_cvt_pk_bf16_f32 v51, v54, v55
	v_lshl_add_u64 v[52:53], v[52:53], 0, v[164:165]
	ds_read_b32 v54, v191
	ds_read_b32 v55, v191 offset:1028
	ds_read_b32 v56, v191 offset:2056
	ds_read_b32 v57, v191 offset:3084
	ds_read_b32 v58, v191 offset:4112
	ds_read_b32 v59, v191 offset:5140
	ds_read_b32 v94, v191 offset:6168
	ds_read_b32 v95, v191 offset:7196
	global_store_dwordx4 v[52:53], v[48:51], off nt
	v_add_u32_e32 v52, s21, v152
	v_lshlrev_b32_e32 v53, 1, v52
	v_and_b32_e32 v53, 0xffffff00, v53
	v_add_u32_e32 v53, s19, v53
	v_or_b32_e32 v53, v53, v192
	v_cndmask_b32_e32 v52, v53, v52, vcc
	v_mad_i64_i32 v[52:53], s[30:31], s20, v52, 0
	v_lshl_add_u64 v[52:53], v[52:53], 1, s[4:5]
	v_lshl_add_u64 v[52:53], v[52:53], 0, s[28:29]
	s_waitcnt lgkmcnt(6)
	v_cvt_pk_bf16_f32 v48, v54, v55
	s_waitcnt lgkmcnt(4)
	v_cvt_pk_bf16_f32 v49, v56, v57
	s_waitcnt lgkmcnt(2)
	v_cvt_pk_bf16_f32 v50, v58, v59
	s_waitcnt lgkmcnt(0)
	v_cvt_pk_bf16_f32 v51, v94, v95
	v_lshl_add_u64 v[52:53], v[52:53], 0, v[164:165]
	ds_read_b32 v54, v194
	ds_read_b32 v55, v194 offset:1028
	ds_read_b32 v56, v194 offset:2056
	ds_read_b32 v57, v194 offset:3084
	ds_read_b32 v58, v194 offset:4112
	ds_read_b32 v59, v194 offset:5140
	ds_read_b32 v94, v194 offset:6168
	ds_read_b32 v95, v194 offset:7196
	global_store_dwordx4 v[52:53], v[48:51], off nt
	v_add_u32_e32 v52, s21, v154
	v_lshlrev_b32_e32 v53, 1, v52
	v_and_b32_e32 v53, 0xffffff00, v53
	v_add_u32_e32 v53, s19, v53
	v_or_b32_e32 v53, v53, v195
	v_cndmask_b32_e32 v52, v53, v52, vcc
	v_mad_i64_i32 v[52:53], s[30:31], s20, v52, 0
	v_lshl_add_u64 v[52:53], v[52:53], 1, s[4:5]
	v_lshl_add_u64 v[52:53], v[52:53], 0, s[28:29]
	s_waitcnt lgkmcnt(6)
	v_cvt_pk_bf16_f32 v48, v54, v55
	s_waitcnt lgkmcnt(4)
	v_cvt_pk_bf16_f32 v49, v56, v57
	s_waitcnt lgkmcnt(2)
	v_cvt_pk_bf16_f32 v50, v58, v59
	s_waitcnt lgkmcnt(0)
	v_cvt_pk_bf16_f32 v51, v94, v95
	v_lshl_add_u64 v[52:53], v[52:53], 0, v[164:165]
	ds_read_b32 v54, v197
	ds_read_b32 v55, v197 offset:1028
	ds_read_b32 v56, v197 offset:2056
	ds_read_b32 v57, v197 offset:3084
	ds_read_b32 v58, v197 offset:4112
	ds_read_b32 v59, v197 offset:5140
	ds_read_b32 v94, v197 offset:6168
	ds_read_b32 v95, v197 offset:7196
	global_store_dwordx4 v[52:53], v[48:51], off nt
	v_add_u32_e32 v52, s21, v156
	v_lshlrev_b32_e32 v53, 1, v52
	v_and_b32_e32 v53, 0xffffff00, v53
	v_add_u32_e32 v53, s19, v53
	v_or_b32_e32 v53, v53, v198
	v_cndmask_b32_e32 v52, v53, v52, vcc
	v_mad_i64_i32 v[52:53], s[20:21], s20, v52, 0
	v_lshl_add_u64 v[52:53], v[52:53], 1, s[4:5]
	s_add_i32 s4, s56, 6
	s_mul_hi_i32 s5, s4, 0x2aaaaaab
	s_lshr_b32 s19, s5, 31
	s_ashr_i32 s5, s5, 4
	s_add_i32 s20, s5, s19
	s_mul_i32 s5, s20, 0x60
	v_lshl_add_u64 v[52:53], v[52:53], 0, s[28:29]
	s_sub_i32 s19, s4, s5
	s_waitcnt lgkmcnt(6)
	v_cvt_pk_bf16_f32 v48, v54, v55
	s_waitcnt lgkmcnt(4)
	v_cvt_pk_bf16_f32 v49, v56, v57
	s_waitcnt lgkmcnt(2)
	v_cvt_pk_bf16_f32 v50, v58, v59
	s_waitcnt lgkmcnt(0)
	v_cvt_pk_bf16_f32 v51, v94, v95
	v_lshl_add_u64 v[52:53], v[52:53], 0, v[164:165]
	s_cmp_lt_i32 s19, 64
	s_mov_b64 s[34:35], -1
	global_store_dwordx4 v[52:53], v[48:51], off nt
	s_barrier
	s_cbranch_scc1 .LBB0_1828
	s_ashr_i32 s21, s20, 31
	s_lshl_b64 s[4:5], s[20:21], 21
	s_add_u32 s30, s54, s4
	s_addc_u32 s31, s55, s5
	s_lshl_b32 s4, s19, 4
	s_add_i32 s4, s4, 0x7ffffc00
	s_and_b32 s28, s4, 0x7fffffc0
	s_lshl_b64 s[4:5], s[20:21], 20
	s_add_u32 s4, s77, s4
	s_addc_u32 s5, s78, s5
	s_mov_b64 s[34:35], 0

; #define LAS __attribute__((address_space(3)))
; DI unsigned pk2(float lo, float hi) { f32x2 v = {lo, hi}; return __builtin_bit_cast(unsigned, __builtin_convertvector(v, bf16v2)); }
; DI void conv_load(const ConvItem& c, f32x4 (&v)[8], int tid) {
; #pragma unroll
;     for (int i = 0; i < 8; ++i) { const int idx = tid + 512 * i, row = idx >> 6, c4 = idx & 63; v[i] = *(const f32x4*)(c.src + (size_t)(c.k0 + row) * c.ld + c.n0 + 4 * c4); }
; }
; DI void conv_store(const ConvItem& c, const f32x4 (&v)[8], LAS float* scr, int tid) {
; #pragma unroll
;     for (int i = 0; i < 8; ++i) { const int idx = tid + 512 * i, row = idx >> 6, c4 = idx & 63; LAS float* d = scr + row * 257 + 4 * c4; d[0] = v[i].x; d[1] = v[i].y; d[2] = v[i].z; d[3] = v[i].w; }
;     __syncthreads();
; #pragma unroll
;     for (int i = 0; i < 4; ++i) { const int idx = tid + 512 * i, n = idx >> 3, cc = idx & 7; const LAS float* sp = scr + (8 * cc) * 257 + n;
;         u32x4 o; o.x = pk2(sp[0], sp[257]); o.y = pk2(sp[2 * 257], sp[3 * 257]); o.z = pk2(sp[4 * 257], sp[5 * 257]); o.w = pk2(sp[6 * 257], sp[7 * 257]);
;         const int h = c.n0 + n; const int drow = (c.mode == 2) ? h : ((h >> 7) * 256 + c.mode * 128 + (h & 127));
;         *(u32x4*)(c.dst + (size_t)drow * c.Kd + c.k0 + 8 * cc) = o; }
;     __syncthreads();
.LBB0_1831:
	v_add_u32_e32 v48, s28, v157
	v_add_u32_e32 v50, s28, v163
	v_add_u32_e32 v52, s28, v177
	v_mad_i64_i32 v[48:49], s[58:59], s34, v48, 0
	v_mad_i64_i32 v[50:51], s[58:59], s34, v50, 0
	v_mad_i64_i32 v[52:53], s[58:59], s34, v52, 0
	v_add_u32_e32 v54, s28, v179
	v_lshl_add_u64 v[48:49], v[48:49], 2, s[30:31]
	s_lshl_b32 s44, s21, 2
	v_lshl_add_u64 v[50:51], v[50:51], 2, s[30:31]
	v_lshl_add_u64 v[52:53], v[52:53], 2, s[30:31]
	v_mad_i64_i32 v[54:55], s[58:59], s34, v54, 0
	v_lshl_add_u64 v[48:49], v[48:49], 0, s[44:45]
	v_lshl_add_u64 v[50:51], v[50:51], 0, s[44:45]
	v_lshl_add_u64 v[52:53], v[52:53], 0, s[44:45]
	v_lshl_add_u64 v[54:55], v[54:55], 2, s[30:31]
	v_lshl_add_u64 v[48:49], v[48:49], 0, v[64:65]
	v_lshl_add_u64 v[50:51], v[50:51], 0, v[64:65]
	v_lshl_add_u64 v[52:53], v[52:53], 0, v[64:65]
	v_lshl_add_u64 v[54:55], v[54:55], 0, s[44:45]
	global_load_dwordx4 v[56:59], v[48:49], off nt
	s_nop 0
	global_load_dwordx4 v[48:51], v[50:51], off nt
	v_lshl_add_u64 v[54:55], v[54:55], 0, v[64:65]
	global_load_dwordx4 v[102:105], v[52:53], off nt
	global_load_dwordx4 v[94:97], v[54:55], off nt
	v_add_u32_e32 v52, s28, v181
	v_mad_i64_i32 v[52:53], s[58:59], s34, v52, 0
	v_add_u32_e32 v54, s28, v183
	v_lshl_add_u64 v[52:53], v[52:53], 2, s[30:31]
	v_mad_i64_i32 v[54:55], s[58:59], s34, v54, 0
	v_lshl_add_u64 v[52:53], v[52:53], 0, s[44:45]
	v_lshl_add_u64 v[54:55], v[54:55], 2, s[30:31]
	v_lshl_add_u64 v[52:53], v[52:53], 0, v[64:65]
	v_lshl_add_u64 v[54:55], v[54:55], 0, s[44:45]
	v_lshl_add_u64 v[54:55], v[54:55], 0, v[64:65]
	global_load_dwordx4 v[118:121], v[52:53], off nt
	global_load_dwordx4 v[110:113], v[54:55], off nt
	v_add_u32_e32 v52, s28, v185
	v_mad_i64_i32 v[52:53], s[58:59], s34, v52, 0
	v_add_u32_e32 v54, s28, v187
	v_lshl_add_u64 v[52:53], v[52:53], 2, s[30:31]
	v_mad_i64_i32 v[54:55], s[34:35], s34, v54, 0
	v_lshl_add_u64 v[52:53], v[52:53], 0, s[44:45]
	v_lshl_add_u64 v[54:55], v[54:55], 2, s[30:31]
	v_lshl_add_u64 v[52:53], v[52:53], 0, v[64:65]
	v_lshl_add_u64 v[54:55], v[54:55], 0, s[44:45]
	v_lshl_add_u64 v[54:55], v[54:55], 0, v[64:65]
	global_load_dwordx4 v[134:137], v[52:53], off nt
	global_load_dwordx4 v[126:129], v[54:55], off nt
	s_waitcnt vmcnt(31)
	ds_write2_b32 v236, v8, v9 offset1:1
	ds_write2_b32 v236, v10, v11 offset0:2 offset1:3
	s_waitcnt vmcnt(30)
	ds_write2_b32 v237, v0, v1 offset1:1
	ds_write2_b32 v237, v2, v3 offset0:2 offset1:3
	s_waitcnt vmcnt(29)
	ds_write2_b32 v238, v24, v25 offset1:1
	ds_write2_b32 v238, v26, v27 offset0:2 offset1:3
	s_waitcnt vmcnt(28)
	ds_write2_b32 v239, v16, v17 offset1:1
	ds_write2_b32 v239, v18, v19 offset0:2 offset1:3
	s_waitcnt vmcnt(27)
	ds_write2_b32 v240, v40, v41 offset1:1
	ds_write2_b32 v240, v42, v43 offset0:2 offset1:3
	s_waitcnt vmcnt(26)
	ds_write2_b32 v241, v32, v33 offset1:1
	ds_write2_b32 v241, v34, v35 offset0:2 offset1:3
	s_waitcnt vmcnt(25)
	ds_write2_b32 v242, v86, v87 offset1:1
	ds_write2_b32 v242, v88, v89 offset0:2 offset1:3
	s_waitcnt vmcnt(24)
	ds_write2_b32 v243, v60, v61 offset1:1
	ds_write2_b32 v243, v62, v63 offset0:2 offset1:3
	s_waitcnt lgkmcnt(0)
	s_barrier
	ds_read_b32 v0, v188
	ds_read_b32 v1, v188 offset:1028
	ds_read_b32 v2, v188 offset:2056
	ds_read_b32 v3, v188 offset:3084
	ds_read_b32 v8, v188 offset:4112
	ds_read_b32 v9, v188 offset:5140
	ds_read_b32 v10, v188 offset:6168
	ds_read_b32 v11, v188 offset:7196
	s_cmp_eq_u32 s25, 2
	s_cselect_b64 vcc, -1, 0
	s_lshl_b32 s19, s25, 7
	s_waitcnt lgkmcnt(6)
	v_cvt_pk_bf16_f32 v0, v0, v1
	s_waitcnt lgkmcnt(4)
	v_cvt_pk_bf16_f32 v1, v2, v3
	s_waitcnt lgkmcnt(2)
	v_cvt_pk_bf16_f32 v2, v8, v9
	v_add_u32_e32 v8, s19, v190
	v_cndmask_b32_e32 v8, v8, v150, vcc
	v_mad_i64_i32 v[8:9], s[30:31], s22, v8, 0
	s_mov_b32 s25, s45
	v_lshl_add_u64 v[8:9], v[8:9], 1, s[6:7]
	s_lshl_b64 s[24:25], s[24:25], 1
	v_lshl_add_u64 v[8:9], v[8:9], 0, s[24:25]
	v_mov_b32_e32 v165, v65
	s_waitcnt lgkmcnt(0)
	v_cvt_pk_bf16_f32 v3, v10, v11
	v_lshl_add_u64 v[8:9], v[8:9], 0, v[164:165]
	ds_read_b32 v10, v191
	ds_read_b32 v11, v191 offset:1028
	ds_read_b32 v16, v191 offset:2056
	ds_read_b32 v17, v191 offset:3084
	ds_read_b32 v18, v191 offset:4112
	ds_read_b32 v19, v191 offset:5140
	ds_read_b32 v24, v191 offset:6168
	ds_read_b32 v25, v191 offset:7196
	global_store_dwordx4 v[8:9], v[0:3], off nt
	v_add_u32_e32 v8, s19, v193
	v_cndmask_b32_e32 v8, v8, v152, vcc
	v_mad_i64_i32 v[8:9], s[30:31], s22, v8, 0
	v_lshl_add_u64 v[8:9], v[8:9], 1, s[6:7]
	v_lshl_add_u64 v[8:9], v[8:9], 0, s[24:25]
	s_waitcnt lgkmcnt(6)
	v_cvt_pk_bf16_f32 v0, v10, v11
	s_waitcnt lgkmcnt(4)
	v_cvt_pk_bf16_f32 v1, v16, v17
	s_waitcnt lgkmcnt(2)
	v_cvt_pk_bf16_f32 v2, v18, v19
	s_waitcnt lgkmcnt(0)
	v_cvt_pk_bf16_f32 v3, v24, v25
	v_lshl_add_u64 v[8:9], v[8:9], 0, v[164:165]
	ds_read_b32 v10, v194
	ds_read_b32 v11, v194 offset:1028
	ds_read_b32 v16, v194 offset:2056
	ds_read_b32 v17, v194 offset:3084
	ds_read_b32 v18, v194 offset:4112
	ds_read_b32 v19, v194 offset:5140
	ds_read_b32 v24, v194 offset:6168
	ds_read_b32 v25, v194 offset:7196
	global_store_dwordx4 v[8:9], v[0:3], off nt
	v_add_u32_e32 v8, s19, v196
	v_cndmask_b32_e32 v8, v8, v154, vcc
	v_mad_i64_i32 v[8:9], s[30:31], s22, v8, 0
	v_lshl_add_u64 v[8:9], v[8:9], 1, s[6:7]
	v_lshl_add_u64 v[8:9], v[8:9], 0, s[24:25]
	s_waitcnt lgkmcnt(6)
	v_cvt_pk_bf16_f32 v0, v10, v11
	s_waitcnt lgkmcnt(4)
	v_cvt_pk_bf16_f32 v1, v16, v17
	s_waitcnt lgkmcnt(2)
	v_cvt_pk_bf16_f32 v2, v18, v19
	s_waitcnt lgkmcnt(0)
	v_cvt_pk_bf16_f32 v3, v24, v25
	v_lshl_add_u64 v[8:9], v[8:9], 0, v[164:165]
	ds_read_b32 v10, v197
	ds_read_b32 v11, v197 offset:1028
	ds_read_b32 v16, v197 offset:2056
	ds_read_b32 v17, v197 offset:3084
	ds_read_b32 v18, v197 offset:4112
	ds_read_b32 v19, v197 offset:5140
	ds_read_b32 v24, v197 offset:6168
	ds_read_b32 v25, v197 offset:7196
	global_store_dwordx4 v[8:9], v[0:3], off nt
	v_add_u32_e32 v8, s19, v199
	v_cndmask_b32_e32 v8, v8, v156, vcc
	v_mad_i64_i32 v[8:9], s[22:23], s22, v8, 0
	v_lshl_add_u64 v[8:9], v[8:9], 1, s[6:7]
	s_add_i32 s6, s56, 7
	s_mul_hi_i32 s7, s6, 0x2aaaaaab
	s_lshr_b32 s19, s7, 31
	s_ashr_i32 s7, s7, 4
	s_add_i32 s22, s7, s19
	s_mul_i32 s7, s22, 0x60
	v_lshl_add_u64 v[8:9], v[8:9], 0, s[24:25]
	s_sub_i32 s19, s6, s7
	s_waitcnt lgkmcnt(6)
	v_cvt_pk_bf16_f32 v0, v10, v11
	s_waitcnt lgkmcnt(4)
	v_cvt_pk_bf16_f32 v1, v16, v17
	s_waitcnt lgkmcnt(2)
	v_cvt_pk_bf16_f32 v2, v18, v19
	s_waitcnt lgkmcnt(0)
	v_cvt_pk_bf16_f32 v3, v24, v25
	v_lshl_add_u64 v[8:9], v[8:9], 0, v[164:165]
	s_cmp_lt_i32 s19, 64
	s_mov_b64 s[34:35], -1
	global_store_dwordx4 v[8:9], v[0:3], off nt
	s_barrier
	s_cbranch_scc1 .LBB0_1833
	s_ashr_i32 s23, s22, 31
	s_lshl_b64 s[6:7], s[22:23], 21
	s_add_u32 s24, s54, s6
	s_addc_u32 s25, s55, s7
	s_lshl_b32 s6, s19, 4
	s_add_i32 s6, s6, 0x7ffffc00
	s_and_b32 s30, s6, 0x7fffffc0
	s_lshl_b64 s[6:7], s[22:23], 20
	s_add_u32 s6, s77, s6
	s_addc_u32 s7, s78, s7
	s_mov_b64 s[34:35], 0

; #define LAS __attribute__((address_space(3)))
; DI unsigned pk2(float lo, float hi) { f32x2 v = {lo, hi}; return __builtin_bit_cast(unsigned, __builtin_convertvector(v, bf16v2)); }
; DI void conv_load(const ConvItem& c, f32x4 (&v)[8], int tid) {
; #pragma unroll
;     for (int i = 0; i < 8; ++i) { const int idx = tid + 512 * i, row = idx >> 6, c4 = idx & 63; v[i] = *(const f32x4*)(c.src + (size_t)(c.k0 + row) * c.ld + c.n0 + 4 * c4); }
; }
; DI void conv_store(const ConvItem& c, const f32x4 (&v)[8], LAS float* scr, int tid) {
; #pragma unroll
;     for (int i = 0; i < 8; ++i) { const int idx = tid + 512 * i, row = idx >> 6, c4 = idx & 63; LAS float* d = scr + row * 257 + 4 * c4; d[0] = v[i].x; d[1] = v[i].y; d[2] = v[i].z; d[3] = v[i].w; }
;     __syncthreads();
; #pragma unroll
;     for (int i = 0; i < 4; ++i) { const int idx = tid + 512 * i, n = idx >> 3, cc = idx & 7; const LAS float* sp = scr + (8 * cc) * 257 + n;
;         u32x4 o; o.x = pk2(sp[0], sp[257]); o.y = pk2(sp[2 * 257], sp[3 * 257]); o.z = pk2(sp[4 * 257], sp[5 * 257]); o.w = pk2(sp[6 * 257], sp[7 * 257]);
;         const int h = c.n0 + n; const int drow = (c.mode == 2) ? h : ((h >> 7) * 256 + c.mode * 128 + (h & 127));
;         *(u32x4*)(c.dst + (size_t)drow * c.Kd + c.k0 + 8 * cc) = o; }
;     __syncthreads();
.LBB0_1836:
	v_add_u32_e32 v0, s30, v157
	v_mad_i64_i32 v[0:1], s[58:59], s34, v0, 0
	v_add_u32_e32 v2, s30, v163
	v_lshl_add_u64 v[0:1], v[0:1], 2, s[24:25]
	s_lshl_b32 s44, s23, 2
	v_mad_i64_i32 v[2:3], s[58:59], s34, v2, 0
	v_lshl_add_u64 v[0:1], v[0:1], 0, s[44:45]
	v_lshl_add_u64 v[2:3], v[2:3], 2, s[24:25]
	v_lshl_add_u64 v[0:1], v[0:1], 0, v[64:65]
	v_lshl_add_u64 v[2:3], v[2:3], 0, s[44:45]
	v_lshl_add_u64 v[2:3], v[2:3], 0, v[64:65]
	global_load_dwordx4 v[60:63], v[0:1], off nt
	global_load_dwordx4 v[52:55], v[2:3], off nt
	v_add_u32_e32 v0, s30, v177
	v_mad_i64_i32 v[0:1], s[58:59], s34, v0, 0
	v_add_u32_e32 v2, s30, v179
	v_lshl_add_u64 v[0:1], v[0:1], 2, s[24:25]
	v_mad_i64_i32 v[2:3], s[58:59], s34, v2, 0
	v_lshl_add_u64 v[0:1], v[0:1], 0, s[44:45]
	v_lshl_add_u64 v[2:3], v[2:3], 2, s[24:25]
	v_lshl_add_u64 v[0:1], v[0:1], 0, v[64:65]
	v_lshl_add_u64 v[2:3], v[2:3], 0, s[44:45]
	v_lshl_add_u64 v[2:3], v[2:3], 0, v[64:65]
	global_load_dwordx4 v[106:109], v[0:1], off nt
	global_load_dwordx4 v[98:101], v[2:3], off nt
	v_add_u32_e32 v0, s30, v181
	v_mad_i64_i32 v[0:1], s[58:59], s34, v0, 0
	v_add_u32_e32 v2, s30, v183
	v_lshl_add_u64 v[0:1], v[0:1], 2, s[24:25]
	v_mad_i64_i32 v[2:3], s[58:59], s34, v2, 0
	v_lshl_add_u64 v[0:1], v[0:1], 0, s[44:45]
	v_lshl_add_u64 v[2:3], v[2:3], 2, s[24:25]
	v_lshl_add_u64 v[0:1], v[0:1], 0, v[64:65]
	v_lshl_add_u64 v[2:3], v[2:3], 0, s[44:45]
	v_lshl_add_u64 v[2:3], v[2:3], 0, v[64:65]
	global_load_dwordx4 v[122:125], v[0:1], off nt
	global_load_dwordx4 v[114:117], v[2:3], off nt
	v_add_u32_e32 v0, s30, v185
	v_mad_i64_i32 v[0:1], s[58:59], s34, v0, 0
	v_add_u32_e32 v2, s30, v187
	v_lshl_add_u64 v[0:1], v[0:1], 2, s[24:25]
	v_mad_i64_i32 v[2:3], s[34:35], s34, v2, 0
	v_lshl_add_u64 v[0:1], v[0:1], 0, s[44:45]
	v_lshl_add_u64 v[2:3], v[2:3], 2, s[24:25]
	v_lshl_add_u64 v[0:1], v[0:1], 0, v[64:65]
	v_lshl_add_u64 v[2:3], v[2:3], 0, s[44:45]
	v_lshl_add_u64 v[2:3], v[2:3], 0, v[64:65]
	global_load_dwordx4 v[138:141], v[0:1], off nt
	global_load_dwordx4 v[130:133], v[2:3], off nt
	s_waitcnt vmcnt(31)
	ds_write2_b32 v236, v12, v13 offset1:1
	ds_write2_b32 v236, v14, v15 offset0:2 offset1:3
	s_waitcnt vmcnt(30)
	ds_write2_b32 v237, v4, v5 offset1:1
	ds_write2_b32 v237, v6, v7 offset0:2 offset1:3
	s_waitcnt vmcnt(29)
	ds_write2_b32 v238, v28, v29 offset1:1
	ds_write2_b32 v238, v30, v31 offset0:2 offset1:3
	s_waitcnt vmcnt(28)
	ds_write2_b32 v239, v20, v21 offset1:1
	ds_write2_b32 v239, v22, v23 offset0:2 offset1:3
	s_waitcnt vmcnt(27)
	ds_write2_b32 v240, v44, v45 offset1:1
	ds_write2_b32 v240, v46, v47 offset0:2 offset1:3
	s_waitcnt vmcnt(26)
	ds_write2_b32 v241, v36, v37 offset1:1
	ds_write2_b32 v241, v38, v39 offset0:2 offset1:3
	s_waitcnt vmcnt(25)
	ds_write2_b32 v242, v90, v91 offset1:1
	ds_write2_b32 v242, v92, v93 offset0:2 offset1:3
	s_waitcnt vmcnt(24)
	ds_write2_b32 v243, v82, v83 offset1:1
	ds_write2_b32 v243, v84, v85 offset0:2 offset1:3
	s_waitcnt lgkmcnt(0)
	s_barrier
	ds_read_b32 v0, v188
	ds_read_b32 v1, v188 offset:1028
	ds_read_b32 v2, v188 offset:2056
	ds_read_b32 v3, v188 offset:3084
	ds_read_b32 v4, v188 offset:4112
	ds_read_b32 v5, v188 offset:5140
	ds_read_b32 v6, v188 offset:6168
	ds_read_b32 v7, v188 offset:7196
	s_cmp_eq_u32 s27, 2
	s_cselect_b64 vcc, -1, 0
	s_lshl_b32 s19, s27, 7
	s_waitcnt lgkmcnt(6)
	v_cvt_pk_bf16_f32 v0, v0, v1
	s_waitcnt lgkmcnt(4)
	v_cvt_pk_bf16_f32 v1, v2, v3
	s_waitcnt lgkmcnt(2)
	v_cvt_pk_bf16_f32 v2, v4, v5
	v_add_u32_e32 v4, s19, v201
	v_cndmask_b32_e32 v4, v4, v200, vcc
	v_mad_i64_i32 v[4:5], s[24:25], s18, v4, 0
	s_mov_b32 s27, s45
	v_lshl_add_u64 v[4:5], v[4:5], 1, s[2:3]
	s_lshl_b64 s[24:25], s[26:27], 1
	v_lshl_add_u64 v[4:5], v[4:5], 0, s[24:25]
	v_mov_b32_e32 v165, v65
	s_waitcnt lgkmcnt(0)
	v_cvt_pk_bf16_f32 v3, v6, v7
	v_lshl_add_u64 v[4:5], v[4:5], 0, v[164:165]
	ds_read_b32 v6, v191
	ds_read_b32 v7, v191 offset:1028
	ds_read_b32 v8, v191 offset:2056
	ds_read_b32 v9, v191 offset:3084
	ds_read_b32 v10, v191 offset:4112
	ds_read_b32 v11, v191 offset:5140
	ds_read_b32 v12, v191 offset:6168
	ds_read_b32 v13, v191 offset:7196
	global_store_dwordx4 v[4:5], v[0:3], off nt
	v_add_u32_e32 v4, s19, v207
	v_cndmask_b32_e32 v4, v4, v206, vcc
	v_mad_i64_i32 v[4:5], s[26:27], s18, v4, 0
	v_lshl_add_u64 v[4:5], v[4:5], 1, s[2:3]
	v_lshl_add_u64 v[4:5], v[4:5], 0, s[24:25]
	s_waitcnt lgkmcnt(6)
	v_cvt_pk_bf16_f32 v0, v6, v7
	s_waitcnt lgkmcnt(4)
	v_cvt_pk_bf16_f32 v1, v8, v9
	s_waitcnt lgkmcnt(2)
	v_cvt_pk_bf16_f32 v2, v10, v11
	s_waitcnt lgkmcnt(0)
	v_cvt_pk_bf16_f32 v3, v12, v13
	v_lshl_add_u64 v[4:5], v[4:5], 0, v[164:165]
	ds_read_b32 v6, v194
	ds_read_b32 v7, v194 offset:1028
	ds_read_b32 v8, v194 offset:2056
	ds_read_b32 v9, v194 offset:3084
	ds_read_b32 v10, v194 offset:4112
	ds_read_b32 v11, v194 offset:5140
	ds_read_b32 v12, v194 offset:6168
	ds_read_b32 v13, v194 offset:7196
	global_store_dwordx4 v[4:5], v[0:3], off nt
	v_add_u32_e32 v4, s19, v209
	v_cndmask_b32_e32 v4, v4, v208, vcc
	v_mad_i64_i32 v[4:5], s[26:27], s18, v4, 0
	v_lshl_add_u64 v[4:5], v[4:5], 1, s[2:3]
	v_lshl_add_u64 v[4:5], v[4:5], 0, s[24:25]
	s_waitcnt lgkmcnt(6)
	v_cvt_pk_bf16_f32 v0, v6, v7
	s_waitcnt lgkmcnt(4)
	v_cvt_pk_bf16_f32 v1, v8, v9
	s_waitcnt lgkmcnt(2)
	v_cvt_pk_bf16_f32 v2, v10, v11
	s_waitcnt lgkmcnt(0)
	v_cvt_pk_bf16_f32 v3, v12, v13
	v_lshl_add_u64 v[4:5], v[4:5], 0, v[164:165]
	ds_read_b32 v6, v197
	ds_read_b32 v7, v197 offset:1028
	ds_read_b32 v8, v197 offset:2056
	ds_read_b32 v9, v197 offset:3084
	ds_read_b32 v10, v197 offset:4112
	ds_read_b32 v11, v197 offset:5140
	ds_read_b32 v12, v197 offset:6168
	ds_read_b32 v13, v197 offset:7196
	global_store_dwordx4 v[4:5], v[0:3], off nt
	v_add_u32_e32 v4, s19, v211
	v_cndmask_b32_e32 v4, v4, v210, vcc
	v_mad_i64_i32 v[4:5], s[18:19], s18, v4, 0
	v_lshl_add_u64 v[4:5], v[4:5], 1, s[2:3]
	s_add_i32 s2, s56, 8
	s_mul_hi_i32 s3, s2, 0x2aaaaaab
	s_lshr_b32 s18, s3, 31
	s_ashr_i32 s3, s3, 4
	s_add_i32 s18, s3, s18
	s_mul_i32 s3, s18, 0x60
	v_lshl_add_u64 v[4:5], v[4:5], 0, s[24:25]
	s_sub_i32 s44, s2, s3
	s_waitcnt lgkmcnt(6)
	v_cvt_pk_bf16_f32 v0, v6, v7
	s_waitcnt lgkmcnt(4)
	v_cvt_pk_bf16_f32 v1, v8, v9
	s_waitcnt lgkmcnt(2)
	v_cvt_pk_bf16_f32 v2, v10, v11
	s_waitcnt lgkmcnt(0)
	v_cvt_pk_bf16_f32 v3, v12, v13
	v_lshl_add_u64 v[4:5], v[4:5], 0, v[164:165]
	s_cmp_lt_i32 s44, 64
	s_mov_b64 s[34:35], -1
	global_store_dwordx4 v[4:5], v[0:3], off nt
	s_barrier
	s_cbranch_scc1 .LBB0_1838
	s_ashr_i32 s19, s18, 31
	s_lshl_b64 s[2:3], s[18:19], 21
	s_add_u32 s26, s54, s2
	s_addc_u32 s27, s55, s3
	s_lshl_b32 s2, s44, 4
	s_add_i32 s2, s2, 0x7ffffc00
	s_and_b32 s24, s2, 0x7fffffc0
	s_lshl_b64 s[2:3], s[18:19], 20
	s_add_u32 s2, s77, s2
	s_addc_u32 s3, s78, s3
	s_mov_b64 s[34:35], 0

; #define LAS __attribute__((address_space(3)))
; DI unsigned pk2(float lo, float hi) { f32x2 v = {lo, hi}; return __builtin_bit_cast(unsigned, __builtin_convertvector(v, bf16v2)); }
; DI void conv_load(const ConvItem& c, f32x4 (&v)[8], int tid) {
; #pragma unroll
;     for (int i = 0; i < 8; ++i) { const int idx = tid + 512 * i, row = idx >> 6, c4 = idx & 63; v[i] = *(const f32x4*)(c.src + (size_t)(c.k0 + row) * c.ld + c.n0 + 4 * c4); }
; }
; DI void conv_store(const ConvItem& c, const f32x4 (&v)[8], LAS float* scr, int tid) {
; #pragma unroll
;     for (int i = 0; i < 8; ++i) { const int idx = tid + 512 * i, row = idx >> 6, c4 = idx & 63; LAS float* d = scr + row * 257 + 4 * c4; d[0] = v[i].x; d[1] = v[i].y; d[2] = v[i].z; d[3] = v[i].w; }
;     __syncthreads();
; #pragma unroll
;     for (int i = 0; i < 4; ++i) { const int idx = tid + 512 * i, n = idx >> 3, cc = idx & 7; const LAS float* sp = scr + (8 * cc) * 257 + n;
;         u32x4 o; o.x = pk2(sp[0], sp[257]); o.y = pk2(sp[2 * 257], sp[3 * 257]); o.z = pk2(sp[4 * 257], sp[5 * 257]); o.w = pk2(sp[6 * 257], sp[7 * 257]);
;         const int h = c.n0 + n; const int drow = (c.mode == 2) ? h : ((h >> 7) * 256 + c.mode * 128 + (h & 127));
;         *(u32x4*)(c.dst + (size_t)drow * c.Kd + c.k0 + 8 * cc) = o; }
;     __syncthreads();
.LBB0_1841:
	v_add_u32_e32 v0, s24, v157
	v_add_u32_e32 v2, s24, v163
	v_add_u32_e32 v8, s24, v177
	v_mad_i64_i32 v[0:1], s[58:59], s34, v0, 0
	v_mad_i64_i32 v[2:3], s[58:59], s34, v2, 0
	v_mad_i64_i32 v[8:9], s[58:59], s34, v8, 0
	v_add_u32_e32 v10, s24, v179
	v_lshl_add_u64 v[0:1], v[0:1], 2, s[26:27]
	v_lshl_add_u64 v[2:3], v[2:3], 2, s[26:27]
	v_lshl_add_u64 v[8:9], v[8:9], 2, s[26:27]
	v_mad_i64_i32 v[10:11], s[58:59], s34, v10, 0
	v_lshl_add_u64 v[0:1], v[0:1], 0, v[64:65]
	v_lshl_add_u64 v[2:3], v[2:3], 0, v[64:65]
	v_lshl_add_u64 v[8:9], v[8:9], 0, v[64:65]
	v_lshl_add_u64 v[10:11], v[10:11], 2, s[26:27]
	global_load_dwordx4 v[4:7], v[0:1], off nt
	s_nop 0
	global_load_dwordx4 v[0:3], v[2:3], off nt
	v_lshl_add_u64 v[10:11], v[10:11], 0, v[64:65]
	global_load_dwordx4 v[20:23], v[8:9], off nt
	global_load_dwordx4 v[16:19], v[10:11], off nt
	v_add_u32_e32 v8, s24, v181
	v_mad_i64_i32 v[8:9], s[58:59], s34, v8, 0
	v_add_u32_e32 v10, s24, v183
	v_lshl_add_u64 v[8:9], v[8:9], 2, s[26:27]
	v_mad_i64_i32 v[10:11], s[58:59], s34, v10, 0
	v_lshl_add_u64 v[8:9], v[8:9], 0, v[64:65]
	v_lshl_add_u64 v[10:11], v[10:11], 2, s[26:27]
	v_lshl_add_u64 v[10:11], v[10:11], 0, v[64:65]
	global_load_dwordx4 v[36:39], v[8:9], off nt
	global_load_dwordx4 v[32:35], v[10:11], off nt
	v_add_u32_e32 v8, s24, v185
	v_mad_i64_i32 v[8:9], s[58:59], s34, v8, 0
	v_add_u32_e32 v10, s24, v187
	v_lshl_add_u64 v[8:9], v[8:9], 2, s[26:27]
	v_mad_i64_i32 v[10:11], s[34:35], s34, v10, 0
	v_lshl_add_u64 v[8:9], v[8:9], 0, v[64:65]
	v_lshl_add_u64 v[10:11], v[10:11], 2, s[26:27]
	v_lshl_add_u64 v[10:11], v[10:11], 0, v[64:65]
	global_load_dwordx4 v[86:89], v[8:9], off nt
	global_load_dwordx4 v[82:85], v[10:11], off nt
	s_waitcnt vmcnt(31)
	ds_write2_b32 v236, v56, v57 offset1:1
	ds_write2_b32 v236, v58, v59 offset0:2 offset1:3
	s_waitcnt vmcnt(30)
	ds_write2_b32 v237, v48, v49 offset1:1
	ds_write2_b32 v237, v50, v51 offset0:2 offset1:3
	s_waitcnt vmcnt(29)
	ds_write2_b32 v238, v102, v103 offset1:1
	ds_write2_b32 v238, v104, v105 offset0:2 offset1:3
	s_waitcnt vmcnt(28)
	ds_write2_b32 v239, v94, v95 offset1:1
	ds_write2_b32 v239, v96, v97 offset0:2 offset1:3
	s_waitcnt vmcnt(27)
	ds_write2_b32 v240, v118, v119 offset1:1
	ds_write2_b32 v240, v120, v121 offset0:2 offset1:3
	s_waitcnt vmcnt(26)
	ds_write2_b32 v241, v110, v111 offset1:1
	ds_write2_b32 v241, v112, v113 offset0:2 offset1:3
	s_waitcnt vmcnt(25)
	ds_write2_b32 v242, v134, v135 offset1:1
	ds_write2_b32 v242, v136, v137 offset0:2 offset1:3
	s_waitcnt vmcnt(24)
	ds_write2_b32 v243, v126, v127 offset1:1
	ds_write2_b32 v243, v128, v129 offset0:2 offset1:3
	s_waitcnt lgkmcnt(0)
	s_barrier
	ds_read_b32 v8, v188
	ds_read_b32 v9, v188 offset:1028
	ds_read_b32 v10, v188 offset:2056
	ds_read_b32 v11, v188 offset:3084
	ds_read_b32 v12, v188 offset:4112
	ds_read_b32 v13, v188 offset:5140
	ds_read_b32 v14, v188 offset:6168
	ds_read_b32 v15, v188 offset:7196
	s_waitcnt lgkmcnt(6)
	v_cvt_pk_bf16_f32 v8, v8, v9
	s_waitcnt lgkmcnt(4)
	v_cvt_pk_bf16_f32 v9, v10, v11
	s_waitcnt lgkmcnt(2)
	v_cvt_pk_bf16_f32 v10, v12, v13
	v_add_u32_e32 v12, s21, v150
	s_cmp_eq_u32 s29, 2
	v_lshlrev_b32_e32 v13, 1, v12
	s_cselect_b64 vcc, -1, 0
	v_and_b32_e32 v13, 0xffffff00, v13
	s_lshl_b32 s19, s29, 7
	v_add_u32_e32 v13, s19, v13
	v_or_b32_e32 v13, v13, v189
	v_cndmask_b32_e32 v12, v13, v12, vcc
	v_mad_i64_i32 v[12:13], s[26:27], s20, v12, 0
	s_mov_b32 s29, s45
	v_lshl_add_u64 v[12:13], v[12:13], 1, s[4:5]
	s_lshl_b64 s[26:27], s[28:29], 1
	v_lshl_add_u64 v[12:13], v[12:13], 0, s[26:27]
	v_mov_b32_e32 v165, v65
	s_waitcnt lgkmcnt(0)
	v_cvt_pk_bf16_f32 v11, v14, v15
	v_lshl_add_u64 v[12:13], v[12:13], 0, v[164:165]
	ds_read_b32 v14, v191
	ds_read_b32 v15, v191 offset:1028
	ds_read_b32 v24, v191 offset:2056
	ds_read_b32 v25, v191 offset:3084
	ds_read_b32 v26, v191 offset:4112
	ds_read_b32 v27, v191 offset:5140
	ds_read_b32 v28, v191 offset:6168
	ds_read_b32 v29, v191 offset:7196
	global_store_dwordx4 v[12:13], v[8:11], off nt
	v_add_u32_e32 v12, s21, v152
	v_lshlrev_b32_e32 v13, 1, v12
	v_and_b32_e32 v13, 0xffffff00, v13
	v_add_u32_e32 v13, s19, v13
	v_or_b32_e32 v13, v13, v192
	v_cndmask_b32_e32 v12, v13, v12, vcc
	v_mad_i64_i32 v[12:13], s[28:29], s20, v12, 0
	v_lshl_add_u64 v[12:13], v[12:13], 1, s[4:5]
	v_lshl_add_u64 v[12:13], v[12:13], 0, s[26:27]
	s_waitcnt lgkmcnt(6)
	v_cvt_pk_bf16_f32 v8, v14, v15
	s_waitcnt lgkmcnt(4)
	v_cvt_pk_bf16_f32 v9, v24, v25
	s_waitcnt lgkmcnt(2)
	v_cvt_pk_bf16_f32 v10, v26, v27
	s_waitcnt lgkmcnt(0)
	v_cvt_pk_bf16_f32 v11, v28, v29
	v_lshl_add_u64 v[12:13], v[12:13], 0, v[164:165]
	ds_read_b32 v14, v194
	ds_read_b32 v15, v194 offset:1028
	ds_read_b32 v24, v194 offset:2056
	ds_read_b32 v25, v194 offset:3084
	ds_read_b32 v26, v194 offset:4112
	ds_read_b32 v27, v194 offset:5140
	ds_read_b32 v28, v194 offset:6168
	ds_read_b32 v29, v194 offset:7196
	global_store_dwordx4 v[12:13], v[8:11], off nt
	v_add_u32_e32 v12, s21, v154
	v_lshlrev_b32_e32 v13, 1, v12
	v_and_b32_e32 v13, 0xffffff00, v13
	v_add_u32_e32 v13, s19, v13
	v_or_b32_e32 v13, v13, v195
	v_cndmask_b32_e32 v12, v13, v12, vcc
	v_mad_i64_i32 v[12:13], s[28:29], s20, v12, 0
	v_lshl_add_u64 v[12:13], v[12:13], 1, s[4:5]
	v_lshl_add_u64 v[12:13], v[12:13], 0, s[26:27]
	s_waitcnt lgkmcnt(6)
	v_cvt_pk_bf16_f32 v8, v14, v15
	s_waitcnt lgkmcnt(4)
	v_cvt_pk_bf16_f32 v9, v24, v25
	s_waitcnt lgkmcnt(2)
	v_cvt_pk_bf16_f32 v10, v26, v27
	s_waitcnt lgkmcnt(0)
	v_cvt_pk_bf16_f32 v11, v28, v29
	v_lshl_add_u64 v[12:13], v[12:13], 0, v[164:165]
	ds_read_b32 v14, v197
	ds_read_b32 v15, v197 offset:1028
	ds_read_b32 v24, v197 offset:2056
	ds_read_b32 v25, v197 offset:3084
	ds_read_b32 v26, v197 offset:4112
	ds_read_b32 v27, v197 offset:5140
	ds_read_b32 v28, v197 offset:6168
	ds_read_b32 v29, v197 offset:7196
	global_store_dwordx4 v[12:13], v[8:11], off nt
	v_add_u32_e32 v12, s21, v156
	v_lshlrev_b32_e32 v13, 1, v12
	v_and_b32_e32 v13, 0xffffff00, v13
	v_add_u32_e32 v13, s19, v13
	v_or_b32_e32 v13, v13, v198
	v_cndmask_b32_e32 v12, v13, v12, vcc
	v_mad_i64_i32 v[12:13], s[20:21], s20, v12, 0
	v_lshl_add_u64 v[12:13], v[12:13], 1, s[4:5]
	s_add_i32 s4, s56, 9
	s_mul_hi_i32 s5, s4, 0x2aaaaaab
	s_lshr_b32 s19, s5, 31
	s_ashr_i32 s5, s5, 4
	s_add_i32 s20, s5, s19
	s_mul_i32 s5, s20, 0x60
	v_lshl_add_u64 v[12:13], v[12:13], 0, s[26:27]
	s_sub_i32 s19, s4, s5
	s_waitcnt lgkmcnt(6)
	v_cvt_pk_bf16_f32 v8, v14, v15
	s_waitcnt lgkmcnt(4)
	v_cvt_pk_bf16_f32 v9, v24, v25
	s_waitcnt lgkmcnt(2)
	v_cvt_pk_bf16_f32 v10, v26, v27
	s_waitcnt lgkmcnt(0)
	v_cvt_pk_bf16_f32 v11, v28, v29
	v_lshl_add_u64 v[12:13], v[12:13], 0, v[164:165]
	s_cmp_lt_i32 s19, 64
	s_mov_b64 s[34:35], -1
	global_store_dwordx4 v[12:13], v[8:11], off nt
	s_barrier
	s_cbranch_scc1 .LBB0_1843
	s_ashr_i32 s21, s20, 31
	s_lshl_b64 s[4:5], s[20:21], 21
	s_add_u32 s28, s54, s4
	s_addc_u32 s29, s55, s5
	s_lshl_b32 s4, s19, 4
	s_add_i32 s4, s4, 0x7ffffc00
	s_and_b32 s26, s4, 0x7fffffc0
	s_lshl_b64 s[4:5], s[20:21], 20
	s_add_u32 s4, s77, s4
	s_addc_u32 s5, s78, s5
	s_mov_b64 s[34:35], 0

; #define LAS __attribute__((address_space(3)))
; DI void conv_load(const ConvItem& c, f32x4 (&v)[8], int tid) {
; #pragma unroll
;     for (int i = 0; i < 8; ++i) { const int idx = tid + 512 * i, row = idx >> 6, c4 = idx & 63; v[i] = *(const f32x4*)(c.src + (size_t)(c.k0 + row) * c.ld + c.n0 + 4 * c4); }
; }
; DI void conv_store(const ConvItem& c, const f32x4 (&v)[8], LAS float* scr, int tid) {
; #pragma unroll
;     for (int i = 0; i < 8; ++i) { const int idx = tid + 512 * i, row = idx >> 6, c4 = idx & 63; LAS float* d = scr + row * 257 + 4 * c4; d[0] = v[i].x; d[1] = v[i].y; d[2] = v[i].z; d[3] = v[i].w; }
;     __syncthreads();
.LBB0_1846:
	v_add_u32_e32 v8, s26, v157
	v_add_u32_e32 v10, s26, v163
	v_add_u32_e32 v24, s26, v177
	v_add_u32_e32 v26, s26, v179
	v_add_u32_e32 v40, s26, v181
	v_add_u32_e32 v42, s26, v183
	v_add_u32_e32 v48, s26, v185
	v_add_u32_e32 v50, s26, v187
	v_mad_i64_i32 v[8:9], s[58:59], s34, v8, 0
	v_mad_i64_i32 v[10:11], s[58:59], s34, v10, 0
	v_mad_i64_i32 v[24:25], s[58:59], s34, v24, 0
	v_mad_i64_i32 v[26:27], s[58:59], s34, v26, 0
	v_mad_i64_i32 v[40:41], s[58:59], s34, v40, 0
	v_mad_i64_i32 v[42:43], s[58:59], s34, v42, 0
	v_mad_i64_i32 v[48:49], s[58:59], s34, v48, 0
	v_mad_i64_i32 v[50:51], s[34:35], s34, v50, 0
	v_lshl_add_u64 v[8:9], v[8:9], 2, s[28:29]
	v_lshl_add_u64 v[10:11], v[10:11], 2, s[28:29]
	v_lshl_add_u64 v[24:25], v[24:25], 2, s[28:29]
	v_lshl_add_u64 v[26:27], v[26:27], 2, s[28:29]
	v_lshl_add_u64 v[40:41], v[40:41], 2, s[28:29]
	v_lshl_add_u64 v[42:43], v[42:43], 2, s[28:29]
	v_lshl_add_u64 v[48:49], v[48:49], 2, s[28:29]
	v_lshl_add_u64 v[50:51], v[50:51], 2, s[28:29]
	v_lshl_add_u64 v[8:9], v[8:9], 0, v[64:65]
	v_lshl_add_u64 v[10:11], v[10:11], 0, v[64:65]
	v_lshl_add_u64 v[24:25], v[24:25], 0, v[64:65]
	v_lshl_add_u64 v[26:27], v[26:27], 0, v[64:65]
	v_lshl_add_u64 v[40:41], v[40:41], 0, v[64:65]
	v_lshl_add_u64 v[42:43], v[42:43], 0, v[64:65]
	v_lshl_add_u64 v[48:49], v[48:49], 0, v[64:65]
	v_lshl_add_u64 v[50:51], v[50:51], 0, v[64:65]
	global_load_dwordx4 v[12:15], v[8:9], off offset:1024 nt
	s_nop 0
	global_load_dwordx4 v[8:11], v[10:11], off offset:1024 nt
	s_nop 0
	global_load_dwordx4 v[28:31], v[24:25], off offset:1024 nt
	s_nop 0
	global_load_dwordx4 v[24:27], v[26:27], off offset:1024 nt
	s_nop 0
	global_load_dwordx4 v[44:47], v[40:41], off offset:1024 nt
	s_nop 0
	global_load_dwordx4 v[40:43], v[42:43], off offset:1024 nt
	s_nop 0
	global_load_dwordx4 v[56:59], v[48:49], off offset:1024 nt
	s_nop 0
	global_load_dwordx4 v[48:51], v[50:51], off offset:1024 nt
	s_waitcnt vmcnt(31)
	ds_write2_b32 v236, v60, v61 offset1:1
	ds_write2_b32 v236, v62, v63 offset0:2 offset1:3
	s_waitcnt vmcnt(30)
	ds_write2_b32 v237, v52, v53 offset1:1
	ds_write2_b32 v237, v54, v55 offset0:2 offset1:3
	s_waitcnt vmcnt(29)
	ds_write2_b32 v238, v106, v107 offset1:1
	ds_write2_b32 v238, v108, v109 offset0:2 offset1:3
	s_waitcnt vmcnt(28)
	ds_write2_b32 v239, v98, v99 offset1:1
	ds_write2_b32 v239, v100, v101 offset0:2 offset1:3
	s_waitcnt vmcnt(27)
	ds_write2_b32 v240, v122, v123 offset1:1
	ds_write2_b32 v240, v124, v125 offset0:2 offset1:3
	s_waitcnt vmcnt(26)
	ds_write2_b32 v241, v114, v115 offset1:1
	ds_write2_b32 v241, v116, v117 offset0:2 offset1:3
	s_waitcnt vmcnt(25)
	ds_write2_b32 v242, v138, v139 offset1:1
	ds_write2_b32 v242, v140, v141 offset0:2 offset1:3
	s_waitcnt vmcnt(24)
	ds_write2_b32 v243, v130, v131 offset1:1
	ds_write2_b32 v243, v132, v133 offset0:2 offset1:3
	s_waitcnt lgkmcnt(0)
	s_barrier
; #define LAS __attribute__((address_space(3)))
; DI unsigned pk2(float lo, float hi) { f32x2 v = {lo, hi}; return __builtin_bit_cast(unsigned, __builtin_convertvector(v, bf16v2)); }
; DI ConvItem conv_item(int it, const float* wg, const float* wu, const float* wdn, bf16_t* we, bf16_t* wd) {
;     ConvItem c; const int e = it / 96; int r = it % 96;
;     if (r < 64) { const int up = r >> 5; r &= 31; c.src = (up ? wu : wg) + (size_t)e * DM * DEXP; c.ld = DEXP; c.k0 = (r >> 1) * 64; c.n0 = (r & 1) * 256; c.dst = we + (size_t)e * 1024 * 1024; c.Kd = 1024; c.mode = up; }
;     else { r -= 64; c.src = wdn + (size_t)e * DEXP * DM; c.ld = DM; c.k0 = (r >> 2) * 64; c.n0 = (r & 3) * 256; c.dst = wd + (size_t)e * 1024 * 512; c.Kd = 512; c.mode = 2; }
; DI void conv_store(const ConvItem& c, const f32x4 (&v)[8], LAS float* scr, int tid) {
;     ...
;     for (int i = 0; i < 4; ++i) { const int idx = tid + 512 * i, n = idx >> 3, cc = idx & 7; const LAS float* sp = scr + (8 * cc) * 257 + n;
;         u32x4 o; o.x = pk2(sp[0], sp[257]); o.y = pk2(sp[2 * 257], sp[3 * 257]); o.z = pk2(sp[4 * 257], sp[5 * 257]); o.w = pk2(sp[6 * 257], sp[7 * 257]);
;         const int h = c.n0 + n; const int drow = (c.mode == 2) ? h : ((h >> 7) * 256 + c.mode * 128 + (h & 127));
;         *(u32x4*)(c.dst + (size_t)drow * c.Kd + c.k0 + 8 * cc) = o; }
;     __syncthreads();
	ds_read_b32 v52, v188
	ds_read_b32 v53, v188 offset:1028
	ds_read_b32 v54, v188 offset:2056
	ds_read_b32 v55, v188 offset:3084
	ds_read_b32 v60, v188 offset:4112
	ds_read_b32 v61, v188 offset:5140
	ds_read_b32 v62, v188 offset:6168
	ds_read_b32 v63, v188 offset:7196
	s_waitcnt lgkmcnt(6)
	v_cvt_pk_bf16_f32 v52, v52, v53
	s_waitcnt lgkmcnt(4)
	v_cvt_pk_bf16_f32 v53, v54, v55
	s_waitcnt lgkmcnt(2)
	v_cvt_pk_bf16_f32 v54, v60, v61
	v_add_u32_e32 v60, s23, v150
	s_cmp_eq_u32 s31, 2
	v_lshlrev_b32_e32 v61, 1, v60
	s_cselect_b64 vcc, -1, 0
	v_and_b32_e32 v61, 0xffffff00, v61
	s_lshl_b32 s19, s31, 7
	v_add_u32_e32 v61, s19, v61
	v_or_b32_e32 v61, v61, v189
	v_cndmask_b32_e32 v60, v61, v60, vcc
	v_mad_i64_i32 v[60:61], s[28:29], s22, v60, 0
	s_mov_b32 s31, s45
	v_lshl_add_u64 v[60:61], v[60:61], 1, s[6:7]
	s_lshl_b64 s[28:29], s[30:31], 1
	v_lshl_add_u64 v[60:61], v[60:61], 0, s[28:29]
	v_mov_b32_e32 v165, v65
	s_waitcnt lgkmcnt(0)
	v_cvt_pk_bf16_f32 v55, v62, v63
	v_lshl_add_u64 v[60:61], v[60:61], 0, v[164:165]
	ds_read_b32 v62, v191
	ds_read_b32 v63, v191 offset:1028
	ds_read_b32 v90, v191 offset:2056
	ds_read_b32 v91, v191 offset:3084
	ds_read_b32 v92, v191 offset:4112
	ds_read_b32 v93, v191 offset:5140
	ds_read_b32 v94, v191 offset:6168
	ds_read_b32 v95, v191 offset:7196
	global_store_dwordx4 v[60:61], v[52:55], off nt
	v_add_u32_e32 v60, s23, v152
	v_lshlrev_b32_e32 v61, 1, v60
	v_and_b32_e32 v61, 0xffffff00, v61
	v_add_u32_e32 v61, s19, v61
	v_or_b32_e32 v61, v61, v192
	v_cndmask_b32_e32 v60, v61, v60, vcc
	v_mad_i64_i32 v[60:61], s[30:31], s22, v60, 0
	v_lshl_add_u64 v[60:61], v[60:61], 1, s[6:7]
	v_lshl_add_u64 v[60:61], v[60:61], 0, s[28:29]
	s_waitcnt lgkmcnt(6)
	v_cvt_pk_bf16_f32 v52, v62, v63
	s_waitcnt lgkmcnt(4)
	v_cvt_pk_bf16_f32 v53, v90, v91
	s_waitcnt lgkmcnt(2)
	v_cvt_pk_bf16_f32 v54, v92, v93
	s_waitcnt lgkmcnt(0)
	v_cvt_pk_bf16_f32 v55, v94, v95
	v_lshl_add_u64 v[60:61], v[60:61], 0, v[164:165]
	ds_read_b32 v62, v194
	ds_read_b32 v63, v194 offset:1028
	ds_read_b32 v90, v194 offset:2056
	ds_read_b32 v91, v194 offset:3084
	ds_read_b32 v92, v194 offset:4112
	ds_read_b32 v93, v194 offset:5140
	ds_read_b32 v94, v194 offset:6168
	ds_read_b32 v95, v194 offset:7196
	global_store_dwordx4 v[60:61], v[52:55], off nt
	v_add_u32_e32 v60, s23, v154
	v_lshlrev_b32_e32 v61, 1, v60
	v_and_b32_e32 v61, 0xffffff00, v61
	v_add_u32_e32 v61, s19, v61
	v_or_b32_e32 v61, v61, v195
	v_cndmask_b32_e32 v60, v61, v60, vcc
	v_mad_i64_i32 v[60:61], s[30:31], s22, v60, 0
	v_lshl_add_u64 v[60:61], v[60:61], 1, s[6:7]
	v_lshl_add_u64 v[60:61], v[60:61], 0, s[28:29]
	s_waitcnt lgkmcnt(6)
	v_cvt_pk_bf16_f32 v52, v62, v63
	s_waitcnt lgkmcnt(4)
	v_cvt_pk_bf16_f32 v53, v90, v91
	s_waitcnt lgkmcnt(2)
	v_cvt_pk_bf16_f32 v54, v92, v93
	s_waitcnt lgkmcnt(0)
	v_cvt_pk_bf16_f32 v55, v94, v95
	v_lshl_add_u64 v[60:61], v[60:61], 0, v[164:165]
	ds_read_b32 v62, v197
	ds_read_b32 v63, v197 offset:1028
	ds_read_b32 v90, v197 offset:2056
	ds_read_b32 v91, v197 offset:3084
	ds_read_b32 v92, v197 offset:4112
	ds_read_b32 v93, v197 offset:5140
	ds_read_b32 v94, v197 offset:6168
	ds_read_b32 v95, v197 offset:7196
	global_store_dwordx4 v[60:61], v[52:55], off nt
	v_add_u32_e32 v60, s23, v156
	v_lshlrev_b32_e32 v61, 1, v60
	v_and_b32_e32 v61, 0xffffff00, v61
	v_add_u32_e32 v61, s19, v61
	v_or_b32_e32 v61, v61, v198
	v_cndmask_b32_e32 v60, v61, v60, vcc
	v_mad_i64_i32 v[60:61], s[22:23], s22, v60, 0
	v_lshl_add_u64 v[60:61], v[60:61], 1, s[6:7]
	s_add_i32 s6, s56, 10
	s_mul_hi_i32 s7, s6, 0x2aaaaaab
	s_lshr_b32 s19, s7, 31
	s_ashr_i32 s7, s7, 4
	s_add_i32 s22, s7, s19
	s_mul_i32 s7, s22, 0x60
	v_lshl_add_u64 v[60:61], v[60:61], 0, s[28:29]
	s_sub_i32 s19, s6, s7
	s_waitcnt lgkmcnt(6)
	v_cvt_pk_bf16_f32 v52, v62, v63
	s_waitcnt lgkmcnt(4)
	v_cvt_pk_bf16_f32 v53, v90, v91
	s_waitcnt lgkmcnt(2)
	v_cvt_pk_bf16_f32 v54, v92, v93
	s_waitcnt lgkmcnt(0)
	v_cvt_pk_bf16_f32 v55, v94, v95
	v_lshl_add_u64 v[60:61], v[60:61], 0, v[164:165]
	s_cmp_lt_i32 s19, 64
	s_mov_b64 s[34:35], -1
	global_store_dwordx4 v[60:61], v[52:55], off nt
	s_barrier
	s_cbranch_scc1 .LBB0_1848
	s_ashr_i32 s23, s22, 31
	s_lshl_b64 s[6:7], s[22:23], 21
	s_add_u32 s30, s54, s6
	s_addc_u32 s31, s55, s7
	s_lshl_b32 s6, s19, 4
	s_add_i32 s6, s6, 0x7ffffc00
	s_and_b32 s28, s6, 0x7fffffc0
	s_lshl_b64 s[6:7], s[22:23], 20
	s_add_u32 s6, s77, s6
	s_addc_u32 s7, s78, s7
	s_mov_b64 s[34:35], 0

; #define LAS __attribute__((address_space(3)))
; DI unsigned pk2(float lo, float hi) { f32x2 v = {lo, hi}; return __builtin_bit_cast(unsigned, __builtin_convertvector(v, bf16v2)); }
; DI void conv_load(const ConvItem& c, f32x4 (&v)[8], int tid) {
; #pragma unroll
;     for (int i = 0; i < 8; ++i) { const int idx = tid + 512 * i, row = idx >> 6, c4 = idx & 63; v[i] = *(const f32x4*)(c.src + (size_t)(c.k0 + row) * c.ld + c.n0 + 4 * c4); }
; }
; DI void conv_store(const ConvItem& c, const f32x4 (&v)[8], LAS float* scr, int tid) {
; #pragma unroll
;     for (int i = 0; i < 8; ++i) { const int idx = tid + 512 * i, row = idx >> 6, c4 = idx & 63; LAS float* d = scr + row * 257 + 4 * c4; d[0] = v[i].x; d[1] = v[i].y; d[2] = v[i].z; d[3] = v[i].w; }
;     __syncthreads();
; #pragma unroll
;     for (int i = 0; i < 4; ++i) { const int idx = tid + 512 * i, n = idx >> 3, cc = idx & 7; const LAS float* sp = scr + (8 * cc) * 257 + n;
;         u32x4 o; o.x = pk2(sp[0], sp[257]); o.y = pk2(sp[2 * 257], sp[3 * 257]); o.z = pk2(sp[4 * 257], sp[5 * 257]); o.w = pk2(sp[6 * 257], sp[7 * 257]);
;         const int h = c.n0 + n; const int drow = (c.mode == 2) ? h : ((h >> 7) * 256 + c.mode * 128 + (h & 127));
;         *(u32x4*)(c.dst + (size_t)drow * c.Kd + c.k0 + 8 * cc) = o; }
;     __syncthreads();
.LBB0_1851:
	v_add_u32_e32 v52, s28, v157
	v_add_u32_e32 v54, s28, v163
	v_add_u32_e32 v90, s28, v177
	v_add_u32_e32 v92, s28, v179
	v_add_u32_e32 v98, s28, v181
	v_add_u32_e32 v100, s28, v183
	v_add_u32_e32 v106, s28, v185
	v_add_u32_e32 v108, s28, v187
	v_mad_i64_i32 v[52:53], s[58:59], s34, v52, 0
	v_mad_i64_i32 v[54:55], s[58:59], s34, v54, 0
	v_mad_i64_i32 v[90:91], s[58:59], s34, v90, 0
	v_mad_i64_i32 v[92:93], s[58:59], s34, v92, 0
	v_mad_i64_i32 v[98:99], s[58:59], s34, v98, 0
	v_mad_i64_i32 v[100:101], s[58:59], s34, v100, 0
	v_mad_i64_i32 v[106:107], s[58:59], s34, v106, 0
	v_mad_i64_i32 v[108:109], s[34:35], s34, v108, 0
	v_lshl_add_u64 v[52:53], v[52:53], 2, s[30:31]
	s_lshl_b32 s44, s21, 2
	v_lshl_add_u64 v[54:55], v[54:55], 2, s[30:31]
	v_lshl_add_u64 v[90:91], v[90:91], 2, s[30:31]
	v_lshl_add_u64 v[92:93], v[92:93], 2, s[30:31]
	v_lshl_add_u64 v[98:99], v[98:99], 2, s[30:31]
	v_lshl_add_u64 v[100:101], v[100:101], 2, s[30:31]
	v_lshl_add_u64 v[106:107], v[106:107], 2, s[30:31]
	v_lshl_add_u64 v[108:109], v[108:109], 2, s[30:31]
	v_lshl_add_u64 v[52:53], v[52:53], 0, s[44:45]
	v_lshl_add_u64 v[54:55], v[54:55], 0, s[44:45]
	v_lshl_add_u64 v[90:91], v[90:91], 0, s[44:45]
	v_lshl_add_u64 v[92:93], v[92:93], 0, s[44:45]
	v_lshl_add_u64 v[98:99], v[98:99], 0, s[44:45]
	v_lshl_add_u64 v[100:101], v[100:101], 0, s[44:45]
	v_lshl_add_u64 v[106:107], v[106:107], 0, s[44:45]
	v_lshl_add_u64 v[108:109], v[108:109], 0, s[44:45]
	v_lshl_add_u64 v[52:53], v[52:53], 0, v[64:65]
	v_lshl_add_u64 v[54:55], v[54:55], 0, v[64:65]
	v_lshl_add_u64 v[90:91], v[90:91], 0, v[64:65]
	v_lshl_add_u64 v[92:93], v[92:93], 0, v[64:65]
	v_lshl_add_u64 v[98:99], v[98:99], 0, v[64:65]
	v_lshl_add_u64 v[100:101], v[100:101], 0, v[64:65]
	v_lshl_add_u64 v[106:107], v[106:107], 0, v[64:65]
	v_lshl_add_u64 v[108:109], v[108:109], 0, v[64:65]
	global_load_dwordx4 v[60:63], v[52:53], off nt
	s_nop 0
	global_load_dwordx4 v[52:55], v[54:55], off nt
	s_nop 0
	global_load_dwordx4 v[94:97], v[90:91], off nt
	s_nop 0
	global_load_dwordx4 v[90:93], v[92:93], off nt
	s_nop 0
	global_load_dwordx4 v[102:105], v[98:99], off nt
	s_nop 0
	global_load_dwordx4 v[98:101], v[100:101], off nt
	s_nop 0
	global_load_dwordx4 v[110:113], v[106:107], off nt
	s_nop 0
	global_load_dwordx4 v[106:109], v[108:109], off nt
	s_waitcnt vmcnt(31)
	ds_write2_b32 v236, v4, v5 offset1:1
	ds_write2_b32 v236, v6, v7 offset0:2 offset1:3
	s_waitcnt vmcnt(30)
	ds_write2_b32 v237, v0, v1 offset1:1
	ds_write2_b32 v237, v2, v3 offset0:2 offset1:3
	s_waitcnt vmcnt(29)
	ds_write2_b32 v238, v20, v21 offset1:1
	ds_write2_b32 v238, v22, v23 offset0:2 offset1:3
	s_waitcnt vmcnt(28)
	ds_write2_b32 v239, v16, v17 offset1:1
	ds_write2_b32 v239, v18, v19 offset0:2 offset1:3
	s_waitcnt vmcnt(27)
	ds_write2_b32 v240, v36, v37 offset1:1
	ds_write2_b32 v240, v38, v39 offset0:2 offset1:3
	s_waitcnt vmcnt(26)
	ds_write2_b32 v241, v32, v33 offset1:1
	ds_write2_b32 v241, v34, v35 offset0:2 offset1:3
	s_waitcnt vmcnt(25)
	ds_write2_b32 v242, v86, v87 offset1:1
	ds_write2_b32 v242, v88, v89 offset0:2 offset1:3
	s_waitcnt vmcnt(24)
	ds_write2_b32 v243, v82, v83 offset1:1
	ds_write2_b32 v243, v84, v85 offset0:2 offset1:3
	s_waitcnt lgkmcnt(0)
	s_barrier
	ds_read_b32 v0, v188
	ds_read_b32 v1, v188 offset:1028
	ds_read_b32 v2, v188 offset:2056
	ds_read_b32 v3, v188 offset:3084
	ds_read_b32 v4, v188 offset:4112
	ds_read_b32 v5, v188 offset:5140
	ds_read_b32 v6, v188 offset:6168
	ds_read_b32 v7, v188 offset:7196
	s_cmp_eq_u32 s25, 2
	s_cselect_b64 vcc, -1, 0
	s_lshl_b32 s19, s25, 7
	s_waitcnt lgkmcnt(6)
	v_cvt_pk_bf16_f32 v0, v0, v1
	s_waitcnt lgkmcnt(4)
	v_cvt_pk_bf16_f32 v1, v2, v3
	s_waitcnt lgkmcnt(2)
	v_cvt_pk_bf16_f32 v2, v4, v5
	v_add_u32_e32 v4, s19, v190
	v_cndmask_b32_e32 v4, v4, v150, vcc
	v_mad_i64_i32 v[4:5], s[30:31], s18, v4, 0
	s_mov_b32 s25, s45
	v_lshl_add_u64 v[4:5], v[4:5], 1, s[2:3]
	s_lshl_b64 s[24:25], s[24:25], 1
	v_lshl_add_u64 v[4:5], v[4:5], 0, s[24:25]
	v_mov_b32_e32 v165, v65
	s_waitcnt lgkmcnt(0)
	v_cvt_pk_bf16_f32 v3, v6, v7
	v_lshl_add_u64 v[4:5], v[4:5], 0, v[164:165]
	ds_read_b32 v6, v191
	ds_read_b32 v7, v191 offset:1028
	ds_read_b32 v16, v191 offset:2056
	ds_read_b32 v17, v191 offset:3084
	ds_read_b32 v18, v191 offset:4112
	ds_read_b32 v19, v191 offset:5140
	ds_read_b32 v20, v191 offset:6168
	ds_read_b32 v21, v191 offset:7196
	global_store_dwordx4 v[4:5], v[0:3], off nt
	v_add_u32_e32 v4, s19, v193
	v_cndmask_b32_e32 v4, v4, v152, vcc
	v_mad_i64_i32 v[4:5], s[30:31], s18, v4, 0
	v_lshl_add_u64 v[4:5], v[4:5], 1, s[2:3]
	v_lshl_add_u64 v[4:5], v[4:5], 0, s[24:25]
	s_waitcnt lgkmcnt(6)
	v_cvt_pk_bf16_f32 v0, v6, v7
	s_waitcnt lgkmcnt(4)
	v_cvt_pk_bf16_f32 v1, v16, v17
	s_waitcnt lgkmcnt(2)
	v_cvt_pk_bf16_f32 v2, v18, v19
	s_waitcnt lgkmcnt(0)
	v_cvt_pk_bf16_f32 v3, v20, v21
	v_lshl_add_u64 v[4:5], v[4:5], 0, v[164:165]
	ds_read_b32 v6, v194
	ds_read_b32 v7, v194 offset:1028
	ds_read_b32 v16, v194 offset:2056
	ds_read_b32 v17, v194 offset:3084
	ds_read_b32 v18, v194 offset:4112
	ds_read_b32 v19, v194 offset:5140
	ds_read_b32 v20, v194 offset:6168
	ds_read_b32 v21, v194 offset:7196
	global_store_dwordx4 v[4:5], v[0:3], off nt
	v_add_u32_e32 v4, s19, v196
	v_cndmask_b32_e32 v4, v4, v154, vcc
	v_mad_i64_i32 v[4:5], s[30:31], s18, v4, 0
	v_lshl_add_u64 v[4:5], v[4:5], 1, s[2:3]
	v_lshl_add_u64 v[4:5], v[4:5], 0, s[24:25]
	s_waitcnt lgkmcnt(6)
	v_cvt_pk_bf16_f32 v0, v6, v7
	s_waitcnt lgkmcnt(4)
	v_cvt_pk_bf16_f32 v1, v16, v17
	s_waitcnt lgkmcnt(2)
	v_cvt_pk_bf16_f32 v2, v18, v19
	s_waitcnt lgkmcnt(0)
	v_cvt_pk_bf16_f32 v3, v20, v21
	v_lshl_add_u64 v[4:5], v[4:5], 0, v[164:165]
	ds_read_b32 v6, v197
	ds_read_b32 v7, v197 offset:1028
	ds_read_b32 v16, v197 offset:2056
	ds_read_b32 v17, v197 offset:3084
	ds_read_b32 v18, v197 offset:4112
	ds_read_b32 v19, v197 offset:5140
	ds_read_b32 v20, v197 offset:6168
	ds_read_b32 v21, v197 offset:7196
	global_store_dwordx4 v[4:5], v[0:3], off nt
	v_add_u32_e32 v4, s19, v199
	v_cndmask_b32_e32 v4, v4, v156, vcc
	v_mad_i64_i32 v[4:5], s[18:19], s18, v4, 0
	s_add_i32 s56, s56, 11
	v_lshl_add_u64 v[4:5], v[4:5], 1, s[2:3]
	s_mul_hi_i32 s2, s56, 0x2aaaaaab
	s_lshr_b32 s3, s2, 31
	s_ashr_i32 s2, s2, 4
	s_add_i32 s18, s2, s3
	s_mul_i32 s2, s18, 0x60
	v_lshl_add_u64 v[4:5], v[4:5], 0, s[24:25]
	s_sub_i32 s25, s56, s2
	s_waitcnt lgkmcnt(6)
	v_cvt_pk_bf16_f32 v0, v6, v7
	s_waitcnt lgkmcnt(4)
	v_cvt_pk_bf16_f32 v1, v16, v17
	s_waitcnt lgkmcnt(2)
	v_cvt_pk_bf16_f32 v2, v18, v19
	s_waitcnt lgkmcnt(0)
	v_cvt_pk_bf16_f32 v3, v20, v21
	v_lshl_add_u64 v[4:5], v[4:5], 0, v[164:165]
	s_cmp_lt_i32 s25, 64
	s_mov_b64 s[34:35], -1
	global_store_dwordx4 v[4:5], v[0:3], off nt
	s_barrier
	s_cbranch_scc1 .LBB0_1853
	s_ashr_i32 s19, s18, 31
	s_lshl_b64 s[2:3], s[18:19], 21
	s_add_u32 s30, s54, s2
	s_addc_u32 s31, s55, s3
	s_lshl_b32 s2, s25, 4
	s_add_i32 s2, s2, 0x7ffffc00
	s_and_b32 s24, s2, 0x7fffffc0
	s_lshl_b64 s[2:3], s[18:19], 20
	s_add_u32 s2, s77, s2
	s_addc_u32 s3, s78, s3
	s_mov_b64 s[34:35], 0

; #define LAS __attribute__((address_space(3)))
; DI unsigned pk2(float lo, float hi) { f32x2 v = {lo, hi}; return __builtin_bit_cast(unsigned, __builtin_convertvector(v, bf16v2)); }
; DI void conv_load(const ConvItem& c, f32x4 (&v)[8], int tid) {
; #pragma unroll
;     for (int i = 0; i < 8; ++i) { const int idx = tid + 512 * i, row = idx >> 6, c4 = idx & 63; v[i] = *(const f32x4*)(c.src + (size_t)(c.k0 + row) * c.ld + c.n0 + 4 * c4); }
; }
; DI void conv_store(const ConvItem& c, const f32x4 (&v)[8], LAS float* scr, int tid) {
; #pragma unroll
;     for (int i = 0; i < 8; ++i) { const int idx = tid + 512 * i, row = idx >> 6, c4 = idx & 63; LAS float* d = scr + row * 257 + 4 * c4; d[0] = v[i].x; d[1] = v[i].y; d[2] = v[i].z; d[3] = v[i].w; }
;     __syncthreads();
; #pragma unroll
;     for (int i = 0; i < 4; ++i) { const int idx = tid + 512 * i, n = idx >> 3, cc = idx & 7; const LAS float* sp = scr + (8 * cc) * 257 + n;
;         u32x4 o; o.x = pk2(sp[0], sp[257]); o.y = pk2(sp[2 * 257], sp[3 * 257]); o.z = pk2(sp[4 * 257], sp[5 * 257]); o.w = pk2(sp[6 * 257], sp[7 * 257]);
;         const int h = c.n0 + n; const int drow = (c.mode == 2) ? h : ((h >> 7) * 256 + c.mode * 128 + (h & 127));
;         *(u32x4*)(c.dst + (size_t)drow * c.Kd + c.k0 + 8 * cc) = o; }
;     __syncthreads();
.LBB0_1856:
	v_add_u32_e32 v0, s24, v157
	v_add_u32_e32 v2, s24, v163
	v_add_u32_e32 v16, s24, v177
	v_add_u32_e32 v18, s24, v179
	v_add_u32_e32 v32, s24, v181
	v_add_u32_e32 v34, s24, v183
	v_add_u32_e32 v82, s24, v185
	v_add_u32_e32 v84, s24, v187
	v_mad_i64_i32 v[0:1], s[50:51], s34, v0, 0
	v_mad_i64_i32 v[2:3], s[50:51], s34, v2, 0
	v_mad_i64_i32 v[16:17], s[50:51], s34, v16, 0
	v_mad_i64_i32 v[18:19], s[50:51], s34, v18, 0
	v_mad_i64_i32 v[32:33], s[50:51], s34, v32, 0
	v_mad_i64_i32 v[34:35], s[50:51], s34, v34, 0
	v_mad_i64_i32 v[82:83], s[50:51], s34, v82, 0
	v_mad_i64_i32 v[84:85], s[34:35], s34, v84, 0
	v_lshl_add_u64 v[0:1], v[0:1], 2, s[30:31]
	s_lshl_b32 s44, s19, 2
	v_lshl_add_u64 v[2:3], v[2:3], 2, s[30:31]
	v_lshl_add_u64 v[16:17], v[16:17], 2, s[30:31]
	v_lshl_add_u64 v[18:19], v[18:19], 2, s[30:31]
	v_lshl_add_u64 v[32:33], v[32:33], 2, s[30:31]
	v_lshl_add_u64 v[34:35], v[34:35], 2, s[30:31]
	v_lshl_add_u64 v[82:83], v[82:83], 2, s[30:31]
	v_lshl_add_u64 v[84:85], v[84:85], 2, s[30:31]
	v_lshl_add_u64 v[0:1], v[0:1], 0, s[44:45]
	v_lshl_add_u64 v[2:3], v[2:3], 0, s[44:45]
	v_lshl_add_u64 v[16:17], v[16:17], 0, s[44:45]
	v_lshl_add_u64 v[18:19], v[18:19], 0, s[44:45]
	v_lshl_add_u64 v[32:33], v[32:33], 0, s[44:45]
	v_lshl_add_u64 v[34:35], v[34:35], 0, s[44:45]
	v_lshl_add_u64 v[82:83], v[82:83], 0, s[44:45]
	v_lshl_add_u64 v[84:85], v[84:85], 0, s[44:45]
	v_lshl_add_u64 v[0:1], v[0:1], 0, v[64:65]
	v_lshl_add_u64 v[2:3], v[2:3], 0, v[64:65]
	v_lshl_add_u64 v[16:17], v[16:17], 0, v[64:65]
	v_lshl_add_u64 v[18:19], v[18:19], 0, v[64:65]
	v_lshl_add_u64 v[32:33], v[32:33], 0, v[64:65]
	v_lshl_add_u64 v[34:35], v[34:35], 0, v[64:65]
	v_lshl_add_u64 v[82:83], v[82:83], 0, v[64:65]
	v_lshl_add_u64 v[84:85], v[84:85], 0, v[64:65]
	global_load_dwordx4 v[4:7], v[0:1], off nt
	s_nop 0
	global_load_dwordx4 v[0:3], v[2:3], off nt
	s_nop 0
	global_load_dwordx4 v[20:23], v[16:17], off nt
	s_nop 0
	global_load_dwordx4 v[16:19], v[18:19], off nt
	s_nop 0
	global_load_dwordx4 v[36:39], v[32:33], off nt
	s_nop 0
	global_load_dwordx4 v[32:35], v[34:35], off nt
	s_nop 0
	global_load_dwordx4 v[86:89], v[82:83], off nt
	s_nop 0
	global_load_dwordx4 v[82:85], v[84:85], off nt
	s_waitcnt vmcnt(31)
	ds_write2_b32 v236, v12, v13 offset1:1
	ds_write2_b32 v236, v14, v15 offset0:2 offset1:3
	s_waitcnt vmcnt(30)
	ds_write2_b32 v237, v8, v9 offset1:1
	ds_write2_b32 v237, v10, v11 offset0:2 offset1:3
	s_waitcnt vmcnt(29)
	ds_write2_b32 v238, v28, v29 offset1:1
	ds_write2_b32 v238, v30, v31 offset0:2 offset1:3
	s_waitcnt vmcnt(28)
	ds_write2_b32 v239, v24, v25 offset1:1
	ds_write2_b32 v239, v26, v27 offset0:2 offset1:3
	s_waitcnt vmcnt(27)
	ds_write2_b32 v240, v44, v45 offset1:1
	ds_write2_b32 v240, v46, v47 offset0:2 offset1:3
	s_waitcnt vmcnt(26)
	ds_write2_b32 v241, v40, v41 offset1:1
	ds_write2_b32 v241, v42, v43 offset0:2 offset1:3
	s_waitcnt vmcnt(25)
	ds_write2_b32 v242, v56, v57 offset1:1
	ds_write2_b32 v242, v58, v59 offset0:2 offset1:3
	s_waitcnt vmcnt(24)
	ds_write2_b32 v243, v48, v49 offset1:1
	ds_write2_b32 v243, v50, v51 offset0:2 offset1:3
	s_waitcnt lgkmcnt(0)
	s_barrier
	ds_read_b32 v8, v188
	ds_read_b32 v9, v188 offset:1028
	ds_read_b32 v10, v188 offset:2056
	ds_read_b32 v11, v188 offset:3084
	ds_read_b32 v12, v188 offset:4112
	ds_read_b32 v13, v188 offset:5140
	ds_read_b32 v14, v188 offset:6168
	ds_read_b32 v15, v188 offset:7196
	s_cmp_eq_u32 s27, 2
	s_cselect_b64 vcc, -1, 0
	s_lshl_b32 s25, s27, 7
	s_waitcnt lgkmcnt(6)
	v_cvt_pk_bf16_f32 v8, v8, v9
	s_waitcnt lgkmcnt(4)
	v_cvt_pk_bf16_f32 v9, v10, v11
	s_waitcnt lgkmcnt(2)
	v_cvt_pk_bf16_f32 v10, v12, v13
	v_add_u32_e32 v12, s25, v201
	v_cndmask_b32_e32 v12, v12, v200, vcc
	v_mad_i64_i32 v[12:13], s[30:31], s20, v12, 0
	s_mov_b32 s27, s45
	v_lshl_add_u64 v[12:13], v[12:13], 1, s[4:5]
	s_lshl_b64 s[26:27], s[26:27], 1
	v_lshl_add_u64 v[12:13], v[12:13], 0, s[26:27]
	v_mov_b32_e32 v165, v65
	s_waitcnt lgkmcnt(0)
	v_cvt_pk_bf16_f32 v11, v14, v15
	v_lshl_add_u64 v[12:13], v[12:13], 0, v[164:165]
	ds_read_b32 v14, v191
	ds_read_b32 v15, v191 offset:1028
	ds_read_b32 v24, v191 offset:2056
	ds_read_b32 v25, v191 offset:3084
	ds_read_b32 v26, v191 offset:4112
	ds_read_b32 v27, v191 offset:5140
	ds_read_b32 v28, v191 offset:6168
	ds_read_b32 v29, v191 offset:7196
	global_store_dwordx4 v[12:13], v[8:11], off nt
	v_add_u32_e32 v12, s25, v207
	v_cndmask_b32_e32 v12, v12, v206, vcc
	v_mad_i64_i32 v[12:13], s[30:31], s20, v12, 0
	v_lshl_add_u64 v[12:13], v[12:13], 1, s[4:5]
	v_lshl_add_u64 v[12:13], v[12:13], 0, s[26:27]
	s_waitcnt lgkmcnt(6)
	v_cvt_pk_bf16_f32 v8, v14, v15
	s_waitcnt lgkmcnt(4)
	v_cvt_pk_bf16_f32 v9, v24, v25
	s_waitcnt lgkmcnt(2)
	v_cvt_pk_bf16_f32 v10, v26, v27
	s_waitcnt lgkmcnt(0)
	v_cvt_pk_bf16_f32 v11, v28, v29
	v_lshl_add_u64 v[12:13], v[12:13], 0, v[164:165]
	ds_read_b32 v14, v194
	ds_read_b32 v15, v194 offset:1028
	ds_read_b32 v24, v194 offset:2056
	ds_read_b32 v25, v194 offset:3084
	ds_read_b32 v26, v194 offset:4112
	ds_read_b32 v27, v194 offset:5140
	ds_read_b32 v28, v194 offset:6168
	ds_read_b32 v29, v194 offset:7196
	global_store_dwordx4 v[12:13], v[8:11], off nt
	v_add_u32_e32 v12, s25, v209
	v_cndmask_b32_e32 v12, v12, v208, vcc
	v_mad_i64_i32 v[12:13], s[30:31], s20, v12, 0
	v_lshl_add_u64 v[12:13], v[12:13], 1, s[4:5]
	v_lshl_add_u64 v[12:13], v[12:13], 0, s[26:27]
	s_waitcnt lgkmcnt(6)
	v_cvt_pk_bf16_f32 v8, v14, v15
	s_waitcnt lgkmcnt(4)
	v_cvt_pk_bf16_f32 v9, v24, v25
	s_waitcnt lgkmcnt(2)
	v_cvt_pk_bf16_f32 v10, v26, v27
	s_waitcnt lgkmcnt(0)
	v_cvt_pk_bf16_f32 v11, v28, v29
	v_lshl_add_u64 v[12:13], v[12:13], 0, v[164:165]
	ds_read_b32 v14, v197
	ds_read_b32 v15, v197 offset:1028
	ds_read_b32 v24, v197 offset:2056
	ds_read_b32 v25, v197 offset:3084
	ds_read_b32 v26, v197 offset:4112
	ds_read_b32 v27, v197 offset:5140
	ds_read_b32 v28, v197 offset:6168
	ds_read_b32 v29, v197 offset:7196
	global_store_dwordx4 v[12:13], v[8:11], off nt
	v_add_u32_e32 v12, s25, v211
	v_cndmask_b32_e32 v12, v12, v210, vcc
	v_mad_i64_i32 v[12:13], s[30:31], s20, v12, 0
	v_lshl_add_u64 v[12:13], v[12:13], 1, s[4:5]
	v_lshl_add_u64 v[12:13], v[12:13], 0, s[26:27]
	s_waitcnt lgkmcnt(6)
	v_cvt_pk_bf16_f32 v8, v14, v15
	s_waitcnt lgkmcnt(4)
	v_cvt_pk_bf16_f32 v9, v24, v25
	s_waitcnt lgkmcnt(2)
	v_cvt_pk_bf16_f32 v10, v26, v27
	s_waitcnt lgkmcnt(0)
	v_cvt_pk_bf16_f32 v11, v28, v29
	v_lshl_add_u64 v[12:13], v[12:13], 0, v[164:165]
	global_store_dwordx4 v[12:13], v[8:11], off nt
	s_barrier
; #define LAS __attribute__((address_space(3)))
; DI unsigned pk2(float lo, float hi) { f32x2 v = {lo, hi}; return __builtin_bit_cast(unsigned, __builtin_convertvector(v, bf16v2)); }
; DI void conv_store(const ConvItem& c, const f32x4 (&v)[8], LAS float* scr, int tid) {
; #pragma unroll
;     for (int i = 0; i < 8; ++i) { const int idx = tid + 512 * i, row = idx >> 6, c4 = idx & 63; LAS float* d = scr + row * 257 + 4 * c4; d[0] = v[i].x; d[1] = v[i].y; d[2] = v[i].z; d[3] = v[i].w; }
;     __syncthreads();
; #pragma unroll
;     for (int i = 0; i < 4; ++i) { const int idx = tid + 512 * i, n = idx >> 3, cc = idx & 7; const LAS float* sp = scr + (8 * cc) * 257 + n;
;         u32x4 o; o.x = pk2(sp[0], sp[257]); o.y = pk2(sp[2 * 257], sp[3 * 257]); o.z = pk2(sp[4 * 257], sp[5 * 257]); o.w = pk2(sp[6 * 257], sp[7 * 257]);
;         const int h = c.n0 + n; const int drow = (c.mode == 2) ? h : ((h >> 7) * 256 + c.mode * 128 + (h & 127));
;         *(u32x4*)(c.dst + (size_t)drow * c.Kd + c.k0 + 8 * cc) = o; }
;     __syncthreads();
	s_waitcnt vmcnt(23)
	ds_write2_b32 v236, v60, v61 offset1:1
	ds_write2_b32 v236, v62, v63 offset0:2 offset1:3
	s_waitcnt vmcnt(22)
	ds_write2_b32 v237, v52, v53 offset1:1
	ds_write2_b32 v237, v54, v55 offset0:2 offset1:3
	s_waitcnt vmcnt(21)
	ds_write2_b32 v238, v94, v95 offset1:1
	ds_write2_b32 v238, v96, v97 offset0:2 offset1:3
	s_waitcnt vmcnt(20)
	ds_write2_b32 v239, v90, v91 offset1:1
	ds_write2_b32 v239, v92, v93 offset0:2 offset1:3
	s_waitcnt vmcnt(19)
	ds_write2_b32 v240, v102, v103 offset1:1
	ds_write2_b32 v240, v104, v105 offset0:2 offset1:3
	s_waitcnt vmcnt(18)
	ds_write2_b32 v241, v98, v99 offset1:1
	ds_write2_b32 v241, v100, v101 offset0:2 offset1:3
	s_waitcnt vmcnt(17)
	ds_write2_b32 v242, v110, v111 offset1:1
	ds_write2_b32 v242, v112, v113 offset0:2 offset1:3
	s_waitcnt vmcnt(16)
	ds_write2_b32 v243, v106, v107 offset1:1
	ds_write2_b32 v243, v108, v109 offset0:2 offset1:3
	s_waitcnt lgkmcnt(0)
	s_barrier
	ds_read_b32 v8, v188
	ds_read_b32 v9, v188 offset:1028
	ds_read_b32 v10, v188 offset:2056
	ds_read_b32 v11, v188 offset:3084
	ds_read_b32 v12, v188 offset:4112
	ds_read_b32 v13, v188 offset:5140
	ds_read_b32 v14, v188 offset:6168
	ds_read_b32 v15, v188 offset:7196
	s_waitcnt lgkmcnt(6)
	v_cvt_pk_bf16_f32 v8, v8, v9
	s_waitcnt lgkmcnt(4)
	v_cvt_pk_bf16_f32 v9, v10, v11
	s_waitcnt lgkmcnt(2)
	v_cvt_pk_bf16_f32 v10, v12, v13
	v_add_u32_e32 v12, s21, v150
	s_cmp_eq_u32 s29, 2
	v_lshlrev_b32_e32 v13, 1, v12
	s_cselect_b64 vcc, -1, 0
	v_and_b32_e32 v13, 0xffffff00, v13
	s_lshl_b32 s20, s29, 7
	v_add_u32_e32 v13, s20, v13
	v_or_b32_e32 v13, v13, v189
	v_cndmask_b32_e32 v12, v13, v12, vcc
	v_mad_i64_i32 v[12:13], s[4:5], s22, v12, 0
	s_mov_b32 s29, s45
	v_lshl_add_u64 v[12:13], v[12:13], 1, s[6:7]
	s_lshl_b64 s[4:5], s[28:29], 1
	v_lshl_add_u64 v[12:13], v[12:13], 0, s[4:5]
	s_waitcnt lgkmcnt(0)
	v_cvt_pk_bf16_f32 v11, v14, v15
	v_lshl_add_u64 v[12:13], v[12:13], 0, v[164:165]
	ds_read_b32 v14, v191
	ds_read_b32 v15, v191 offset:1028
	ds_read_b32 v24, v191 offset:2056
	ds_read_b32 v25, v191 offset:3084
	ds_read_b32 v26, v191 offset:4112
	ds_read_b32 v27, v191 offset:5140
	ds_read_b32 v28, v191 offset:6168
	ds_read_b32 v29, v191 offset:7196
	global_store_dwordx4 v[12:13], v[8:11], off nt
	v_add_u32_e32 v12, s21, v152
	v_lshlrev_b32_e32 v13, 1, v12
	v_and_b32_e32 v13, 0xffffff00, v13
	v_add_u32_e32 v13, s20, v13
	v_or_b32_e32 v13, v13, v192
	v_cndmask_b32_e32 v12, v13, v12, vcc
	v_mad_i64_i32 v[12:13], s[26:27], s22, v12, 0
	v_lshl_add_u64 v[12:13], v[12:13], 1, s[6:7]
	v_lshl_add_u64 v[12:13], v[12:13], 0, s[4:5]
	s_waitcnt lgkmcnt(6)
	v_cvt_pk_bf16_f32 v8, v14, v15
	s_waitcnt lgkmcnt(4)
	v_cvt_pk_bf16_f32 v9, v24, v25
	s_waitcnt lgkmcnt(2)
	v_cvt_pk_bf16_f32 v10, v26, v27
	s_waitcnt lgkmcnt(0)
	v_cvt_pk_bf16_f32 v11, v28, v29
	v_lshl_add_u64 v[12:13], v[12:13], 0, v[164:165]
	ds_read_b32 v14, v194
	ds_read_b32 v15, v194 offset:1028
	ds_read_b32 v24, v194 offset:2056
	ds_read_b32 v25, v194 offset:3084
	ds_read_b32 v26, v194 offset:4112
	ds_read_b32 v27, v194 offset:5140
	ds_read_b32 v28, v194 offset:6168
	ds_read_b32 v29, v194 offset:7196
	global_store_dwordx4 v[12:13], v[8:11], off nt
	v_add_u32_e32 v12, s21, v154
	v_lshlrev_b32_e32 v13, 1, v12
	v_and_b32_e32 v13, 0xffffff00, v13
	v_add_u32_e32 v13, s20, v13
	v_or_b32_e32 v13, v13, v195
	v_cndmask_b32_e32 v12, v13, v12, vcc
	v_mad_i64_i32 v[12:13], s[26:27], s22, v12, 0
	v_lshl_add_u64 v[12:13], v[12:13], 1, s[6:7]
	v_lshl_add_u64 v[12:13], v[12:13], 0, s[4:5]
	s_waitcnt lgkmcnt(6)
	v_cvt_pk_bf16_f32 v8, v14, v15
	s_waitcnt lgkmcnt(4)
	v_cvt_pk_bf16_f32 v9, v24, v25
	s_waitcnt lgkmcnt(2)
	v_cvt_pk_bf16_f32 v10, v26, v27
	s_waitcnt lgkmcnt(0)
	v_cvt_pk_bf16_f32 v11, v28, v29
	v_lshl_add_u64 v[12:13], v[12:13], 0, v[164:165]
	ds_read_b32 v14, v197
	ds_read_b32 v15, v197 offset:1028
	ds_read_b32 v24, v197 offset:2056
	ds_read_b32 v25, v197 offset:3084
	ds_read_b32 v26, v197 offset:4112
	ds_read_b32 v27, v197 offset:5140
	ds_read_b32 v28, v197 offset:6168
	ds_read_b32 v29, v197 offset:7196
	global_store_dwordx4 v[12:13], v[8:11], off nt
	v_add_u32_e32 v12, s21, v156
	v_lshlrev_b32_e32 v13, 1, v12
	v_and_b32_e32 v13, 0xffffff00, v13
	v_add_u32_e32 v13, s20, v13
	v_or_b32_e32 v13, v13, v198
	v_cndmask_b32_e32 v12, v13, v12, vcc
	v_mad_i64_i32 v[12:13], s[20:21], s22, v12, 0
	v_lshl_add_u64 v[12:13], v[12:13], 1, s[6:7]
	v_lshl_add_u64 v[12:13], v[12:13], 0, s[4:5]
	s_waitcnt lgkmcnt(6)
	v_cvt_pk_bf16_f32 v8, v14, v15
	s_waitcnt lgkmcnt(4)
	v_cvt_pk_bf16_f32 v9, v24, v25
	s_waitcnt lgkmcnt(2)
	v_cvt_pk_bf16_f32 v10, v26, v27
	s_waitcnt lgkmcnt(0)
	v_cvt_pk_bf16_f32 v11, v28, v29
	v_lshl_add_u64 v[12:13], v[12:13], 0, v[164:165]
	global_store_dwordx4 v[12:13], v[8:11], off nt
	s_barrier
; #define LAS __attribute__((address_space(3)))
; DI unsigned pk2(float lo, float hi) { f32x2 v = {lo, hi}; return __builtin_bit_cast(unsigned, __builtin_convertvector(v, bf16v2)); }
; DI void conv_store(const ConvItem& c, const f32x4 (&v)[8], LAS float* scr, int tid) {
; #pragma unroll
;     for (int i = 0; i < 8; ++i) { const int idx = tid + 512 * i, row = idx >> 6, c4 = idx & 63; LAS float* d = scr + row * 257 + 4 * c4; d[0] = v[i].x; d[1] = v[i].y; d[2] = v[i].z; d[3] = v[i].w; }
;     __syncthreads();
; #pragma unroll
;     for (int i = 0; i < 4; ++i) { const int idx = tid + 512 * i, n = idx >> 3, cc = idx & 7; const LAS float* sp = scr + (8 * cc) * 257 + n;
;         u32x4 o; o.x = pk2(sp[0], sp[257]); o.y = pk2(sp[2 * 257], sp[3 * 257]); o.z = pk2(sp[4 * 257], sp[5 * 257]); o.w = pk2(sp[6 * 257], sp[7 * 257]);
;         const int h = c.n0 + n; const int drow = (c.mode == 2) ? h : ((h >> 7) * 256 + c.mode * 128 + (h & 127));
;         *(u32x4*)(c.dst + (size_t)drow * c.Kd + c.k0 + 8 * cc) = o; }
;     __syncthreads();
	s_waitcnt vmcnt(15)
	ds_write2_b32 v236, v4, v5 offset1:1
	ds_write2_b32 v236, v6, v7 offset0:2 offset1:3
	s_waitcnt vmcnt(14)
	ds_write2_b32 v237, v0, v1 offset1:1
	ds_write2_b32 v237, v2, v3 offset0:2 offset1:3
	s_waitcnt vmcnt(13)
	ds_write2_b32 v238, v20, v21 offset1:1
	ds_write2_b32 v238, v22, v23 offset0:2 offset1:3
	s_waitcnt vmcnt(12)
	ds_write2_b32 v239, v16, v17 offset1:1
	ds_write2_b32 v239, v18, v19 offset0:2 offset1:3
	s_waitcnt vmcnt(11)
	ds_write2_b32 v240, v36, v37 offset1:1
	ds_write2_b32 v240, v38, v39 offset0:2 offset1:3
	s_waitcnt vmcnt(10)
	ds_write2_b32 v241, v32, v33 offset1:1
	ds_write2_b32 v241, v34, v35 offset0:2 offset1:3
	s_waitcnt vmcnt(9)
	ds_write2_b32 v242, v86, v87 offset1:1
	ds_write2_b32 v242, v88, v89 offset0:2 offset1:3
	s_waitcnt vmcnt(8)
	ds_write2_b32 v243, v82, v83 offset1:1
	ds_write2_b32 v243, v84, v85 offset0:2 offset1:3
	s_waitcnt lgkmcnt(0)
	s_barrier
	ds_read_b32 v0, v188
	ds_read_b32 v1, v188 offset:1028
	ds_read_b32 v2, v188 offset:2056
	ds_read_b32 v3, v188 offset:3084
	ds_read_b32 v4, v188 offset:4112
	ds_read_b32 v5, v188 offset:5140
	ds_read_b32 v6, v188 offset:6168
	ds_read_b32 v7, v188 offset:7196
	s_waitcnt lgkmcnt(6)
	v_cvt_pk_bf16_f32 v0, v0, v1
	s_waitcnt lgkmcnt(4)
	v_cvt_pk_bf16_f32 v1, v2, v3
	s_waitcnt lgkmcnt(2)
	v_cvt_pk_bf16_f32 v2, v4, v5
	v_add_u32_e32 v4, s19, v150
	s_cmp_eq_u32 s23, 2
	v_lshlrev_b32_e32 v5, 1, v4
	s_cselect_b64 vcc, -1, 0
	v_and_b32_e32 v5, 0xffffff00, v5
	s_lshl_b32 s20, s23, 7
	v_add_u32_e32 v5, s20, v5
	v_or_b32_e32 v5, v5, v189
	v_cndmask_b32_e32 v4, v5, v4, vcc
	v_mad_i64_i32 v[4:5], s[4:5], s18, v4, 0
	s_mov_b32 s25, s45
	v_lshl_add_u64 v[4:5], v[4:5], 1, s[2:3]
	s_lshl_b64 s[4:5], s[24:25], 1
	v_lshl_add_u64 v[4:5], v[4:5], 0, s[4:5]
	s_waitcnt lgkmcnt(0)
	v_cvt_pk_bf16_f32 v3, v6, v7
	v_lshl_add_u64 v[4:5], v[4:5], 0, v[164:165]
	ds_read_b32 v6, v191
	ds_read_b32 v7, v191 offset:1028
	ds_read_b32 v8, v191 offset:2056
	ds_read_b32 v9, v191 offset:3084
	ds_read_b32 v10, v191 offset:4112
	ds_read_b32 v11, v191 offset:5140
	ds_read_b32 v12, v191 offset:6168
	ds_read_b32 v13, v191 offset:7196
	global_store_dwordx4 v[4:5], v[0:3], off nt
	v_add_u32_e32 v4, s19, v152
	v_lshlrev_b32_e32 v5, 1, v4
	v_and_b32_e32 v5, 0xffffff00, v5
	v_add_u32_e32 v5, s20, v5
	v_or_b32_e32 v5, v5, v192
	v_cndmask_b32_e32 v4, v5, v4, vcc
	v_mad_i64_i32 v[4:5], s[6:7], s18, v4, 0
	v_lshl_add_u64 v[4:5], v[4:5], 1, s[2:3]
	v_lshl_add_u64 v[4:5], v[4:5], 0, s[4:5]
	s_waitcnt lgkmcnt(6)
	v_cvt_pk_bf16_f32 v0, v6, v7
	s_waitcnt lgkmcnt(4)
	v_cvt_pk_bf16_f32 v1, v8, v9
	s_waitcnt lgkmcnt(2)
	v_cvt_pk_bf16_f32 v2, v10, v11
	s_waitcnt lgkmcnt(0)
	v_cvt_pk_bf16_f32 v3, v12, v13
	v_lshl_add_u64 v[4:5], v[4:5], 0, v[164:165]
	ds_read_b32 v6, v194
	ds_read_b32 v7, v194 offset:1028
	ds_read_b32 v8, v194 offset:2056
	ds_read_b32 v9, v194 offset:3084
	ds_read_b32 v10, v194 offset:4112
	ds_read_b32 v11, v194 offset:5140
	ds_read_b32 v12, v194 offset:6168
	ds_read_b32 v13, v194 offset:7196
	global_store_dwordx4 v[4:5], v[0:3], off nt
	v_add_u32_e32 v4, s19, v154
	v_lshlrev_b32_e32 v5, 1, v4
	v_and_b32_e32 v5, 0xffffff00, v5
	v_add_u32_e32 v5, s20, v5
	v_or_b32_e32 v5, v5, v195
	v_cndmask_b32_e32 v4, v5, v4, vcc
	v_mad_i64_i32 v[4:5], s[6:7], s18, v4, 0
	v_lshl_add_u64 v[4:5], v[4:5], 1, s[2:3]
	v_lshl_add_u64 v[4:5], v[4:5], 0, s[4:5]
	s_waitcnt lgkmcnt(6)
	v_cvt_pk_bf16_f32 v0, v6, v7
	s_waitcnt lgkmcnt(4)
	v_cvt_pk_bf16_f32 v1, v8, v9
	s_waitcnt lgkmcnt(2)
	v_cvt_pk_bf16_f32 v2, v10, v11
	s_waitcnt lgkmcnt(0)
	v_cvt_pk_bf16_f32 v3, v12, v13
	v_lshl_add_u64 v[4:5], v[4:5], 0, v[164:165]
	ds_read_b32 v6, v197
	ds_read_b32 v7, v197 offset:1028
	ds_read_b32 v8, v197 offset:2056
	ds_read_b32 v9, v197 offset:3084
	ds_read_b32 v10, v197 offset:4112
	ds_read_b32 v11, v197 offset:5140
	ds_read_b32 v12, v197 offset:6168
	ds_read_b32 v13, v197 offset:7196
	global_store_dwordx4 v[4:5], v[0:3], off nt
	v_add_u32_e32 v4, s19, v156
	v_lshlrev_b32_e32 v5, 1, v4
	v_and_b32_e32 v5, 0xffffff00, v5
	v_add_u32_e32 v5, s20, v5
	v_or_b32_e32 v5, v5, v198
	v_cndmask_b32_e32 v4, v5, v4, vcc
	v_mad_i64_i32 v[4:5], s[6:7], s18, v4, 0
	v_lshl_add_u64 v[4:5], v[4:5], 1, s[2:3]
	v_lshl_add_u64 v[4:5], v[4:5], 0, s[4:5]
	s_waitcnt lgkmcnt(6)
	v_cvt_pk_bf16_f32 v0, v6, v7
	s_waitcnt lgkmcnt(4)
	v_cvt_pk_bf16_f32 v1, v8, v9
	s_waitcnt lgkmcnt(2)
	v_cvt_pk_bf16_f32 v2, v10, v11
	s_waitcnt lgkmcnt(0)
	v_cvt_pk_bf16_f32 v3, v12, v13
	v_lshl_add_u64 v[4:5], v[4:5], 0, v[164:165]
	s_mov_b64 s[50:51], 0
	global_store_dwordx4 v[4:5], v[0:3], off nt
	s_barrier
